# attention steps: transposed V reads issued in the order the P.V MFMAs consume them; each MFMA waits only for its own reads (counted lgkmcnt) instead of all 16
# speedup vs baseline: 1.0170x; 1.0087x over previous
.LBB0_1456:
	s_add_i32 s2, s79, 1
	s_and_b32 s2, s2, 3
	s_mulk_i32 s2, 0x3000
	v_add_u32_e32 v72, s2, v168
	ds_read_b128 v[68:71], v72
	ds_read_b128 v[172:175], v72 offset:512
	ds_read_b128 v[176:179], v72 offset:2048
	ds_read_b128 v[180:183], v72 offset:2560
	ds_read_b128 v[184:187], v72 offset:4096
	ds_read_b128 v[190:193], v72 offset:4608
	ds_read_b128 v[212:215], v72 offset:6144
	ds_read_b128 v[216:219], v72 offset:6656
	ds_read_b128 v[224:227], v72 offset:8192
	ds_read_b128 v[228:231], v72 offset:8704
	ds_read_b128 v[232:235], v72 offset:10240
	ds_read_b128 v[236:239], v72 offset:10752
	s_waitcnt lgkmcnt(11)
	v_mfma_f32_32x32x16_bf16 v[100:115], v[68:71], v[116:119], v[36:51]
	v_exp_f32_e32 v84, v84
	v_exp_f32_e32 v85, v85
	v_exp_f32_e32 v86, v86
	v_exp_f32_e32 v87, v87
	s_waitcnt lgkmcnt(10)
	v_mfma_f32_32x32x16_bf16 v[68:83], v[172:175], v[116:119], v[36:51]
	v_add_f32_e64 v172, v84, 0
	v_add_f32_e64 v173, v85, 0
	v_add_f32_e64 v172, v86, v172
	v_add_f32_e64 v173, v87, v173
	s_waitcnt lgkmcnt(9)
	v_mfma_f32_32x32x16_bf16 v[100:115], v[176:179], v[120:123], v[100:115]
	v_exp_f32_e32 v88, v88
	v_exp_f32_e32 v89, v89
	v_exp_f32_e32 v90, v90
	v_exp_f32_e32 v91, v91
	v_pk_add_f32 v[172:173], v[88:89], v[172:173]
	s_nop 0
	v_pk_add_f32 v[172:173], v[90:91], v[172:173]
	s_waitcnt lgkmcnt(8)
	v_mfma_f32_32x32x16_bf16 v[68:83], v[180:183], v[120:123], v[68:83]
	s_waitcnt lgkmcnt(7)
	v_mfma_f32_32x32x16_bf16 v[100:115], v[184:187], v[124:127], v[100:115]
	v_exp_f32_e32 v92, v92
	v_exp_f32_e32 v93, v93
	v_exp_f32_e32 v94, v94
	v_exp_f32_e32 v95, v95
	v_pk_add_f32 v[172:173], v[92:93], v[172:173]
	s_nop 0
	v_pk_add_f32 v[172:173], v[94:95], v[172:173]
	s_waitcnt lgkmcnt(6)
	v_mfma_f32_32x32x16_bf16 v[68:83], v[190:193], v[124:127], v[68:83]
	s_waitcnt lgkmcnt(5)
	v_mfma_f32_32x32x16_bf16 v[100:115], v[212:215], v[128:131], v[100:115]
	v_exp_f32_e32 v96, v96
	v_exp_f32_e32 v97, v97
	v_exp_f32_e32 v98, v98
	v_exp_f32_e32 v99, v99
	v_pk_add_f32 v[172:173], v[96:97], v[172:173]
	s_nop 0
	v_pk_add_f32 v[172:173], v[98:99], v[172:173]
	s_waitcnt lgkmcnt(4)
	v_mfma_f32_32x32x16_bf16 v[68:83], v[216:219], v[128:131], v[68:83]
	v_exp_f32_e32 v174, v52
	v_exp_f32_e32 v175, v53
	s_waitcnt lgkmcnt(3)
	v_mfma_f32_32x32x16_bf16 v[100:115], v[224:227], v[132:135], v[100:115]
	v_add_f32_e64 v52, v174, v172
	v_add_f32_e64 v53, v175, v173
	v_exp_f32_e32 v172, v54
	v_exp_f32_e32 v173, v55
	s_nop 0
	v_pk_add_f32 v[52:53], v[172:173], v[52:53]
	s_waitcnt lgkmcnt(2)
	v_mfma_f32_32x32x16_bf16 v[68:83], v[228:231], v[132:135], v[68:83]
	s_waitcnt lgkmcnt(1)
	v_mfma_f32_32x32x16_bf16 v[100:115], v[232:235], v[136:139], v[100:115]
	v_exp_f32_e32 v176, v56
	v_exp_f32_e32 v177, v57
	v_exp_f32_e32 v178, v58
	v_exp_f32_e32 v179, v59
	v_pk_add_f32 v[52:53], v[176:177], v[52:53]
	s_nop 0
	v_pk_add_f32 v[194:195], v[178:179], v[52:53]
	s_waitcnt lgkmcnt(0)
	v_mfma_f32_32x32x16_bf16 v[68:83], v[236:239], v[136:139], v[68:83]
	s_and_b32 s2, s78, 0x4000
	v_add_u32_e32 v212, s2, v2
	v_cvt_pk_bf16_f32 v54, v88, v89
	ds_read_b64_tr_b16 v[88:89],v212 offset:0
	v_cvt_pk_bf16_f32 v55, v90, v91
	ds_read_b64_tr_b16 v[90:91],v212 offset:512
	v_cvt_pk_bf16_f32 v53, v86, v87
	v_cvt_pk_bf16_f32 v86, v176, v177
	ds_read_b64_tr_b16 v[176:177],v212 offset:4096
	v_cvt_pk_bf16_f32 v87, v178, v179
	ds_read_b64_tr_b16 v[178:179],v212 offset:4608
	v_cvt_pk_bf16_f32 v56, v92, v93
	ds_read_b64_tr_b16 v[92:93],v212 offset:1024
	v_cvt_pk_bf16_f32 v57, v94, v95
	ds_read_b64_tr_b16 v[94:95],v212 offset:1536
	ds_read_b64_tr_b16 v[180:181],v212 offset:5120
	ds_read_b64_tr_b16 v[182:183],v212 offset:5632
	v_cvt_pk_bf16_f32 v58, v96, v97
	ds_read_b64_tr_b16 v[96:97],v212 offset:2048
	v_cvt_pk_bf16_f32 v59, v98, v99
	ds_read_b64_tr_b16 v[98:99],v212 offset:2560
	ds_read_b64_tr_b16 v[184:185],v212 offset:6144
	ds_read_b64_tr_b16 v[186:187],v212 offset:6656
	v_cvt_pk_bf16_f32 v52, v84, v85
	v_cvt_pk_bf16_f32 v85, v172, v173
	ds_read_b64_tr_b16 v[172:173],v212 offset:3072
	v_cvt_pk_bf16_f32 v84, v174, v175
	ds_read_b64_tr_b16 v[174:175],v212 offset:3584
	ds_read_b64_tr_b16 v[190:191],v212 offset:7168
	ds_read_b64_tr_b16 v[192:193],v212 offset:7680
	s_waitcnt lgkmcnt(14)
	v_mfma_f32_32x32x16_bf16 v[4:19], v[52:55], v[88:91], v[4:19]
	s_waitcnt lgkmcnt(12)
	v_mfma_f32_32x32x16_bf16 v[20:35], v[52:55], v[176:179], v[20:35]
	v_exp_f32_e32 v52, v60
	v_exp_f32_e32 v53, v61
	v_exp_f32_e32 v60, v62
	v_exp_f32_e32 v61, v63
	v_pk_add_f32 v[54:55], v[52:53], v[194:195]
	s_nop 0
	v_pk_add_f32 v[54:55], v[60:61], v[54:55]
	s_waitcnt lgkmcnt(10)
	v_mfma_f32_32x32x16_bf16 v[4:19], v[56:59], v[92:95], v[4:19]
	v_cvt_pk_bf16_f32 v52, v52, v53
	v_cvt_pk_bf16_f32 v53, v60, v61
	s_waitcnt lgkmcnt(8)
	v_mfma_f32_32x32x16_bf16 v[20:35], v[56:59], v[180:183], v[20:35]
	v_exp_f32_e32 v56, v64
	v_exp_f32_e32 v57, v65
	v_exp_f32_e32 v58, v66
	v_exp_f32_e32 v59, v67
	v_pk_add_f32 v[54:55], v[56:57], v[54:55]
	s_nop 0
	v_pk_add_f32 v[62:63], v[58:59], v[54:55]
	v_cvt_pk_bf16_f32 v54, v56, v57
	v_add_f32_e32 v56, v62, v63
	v_add_f32_e32 v171, v171, v56
	v_cvt_pk_bf16_f32 v55, v58, v59
	s_waitcnt lgkmcnt(6)
	v_mfma_f32_32x32x16_bf16 v[4:19], v[84:87], v[96:99], v[4:19]
	v_max3_f32 v56, v100, v68, v101
	s_nop 0
	v_max3_f32 v56, v56, v69, v102
	s_nop 0
	v_max3_f32 v56, v56, v70, v103
	s_nop 0
	v_max3_f32 v56, v56, v71, v104
	s_waitcnt lgkmcnt(4)
	v_mfma_f32_32x32x16_bf16 v[20:35], v[84:87], v[184:187], v[20:35]
	v_max3_f32 v56, v56, v72, v105
	s_nop 0
	v_max3_f32 v56, v56, v73, v106
	s_nop 0
	v_max3_f32 v56, v56, v74, v107
	s_nop 0
	v_max3_f32 v56, v56, v75, v107
	s_waitcnt lgkmcnt(2)
	v_mfma_f32_32x32x16_bf16 v[4:19], v[52:55], v[172:175], v[4:19]
	s_waitcnt lgkmcnt(0)
	v_mfma_f32_32x32x16_bf16 v[20:35], v[52:55], v[190:193], v[20:35]
	v_max3_f32 v52, v56, v108, v76
	s_nop 0
	v_max3_f32 v52, v52, v109, v77
	s_nop 0
	v_max3_f32 v52, v52, v110, v78
	s_nop 0
	v_max3_f32 v52, v52, v111, v79
	s_nop 0
	v_max3_f32 v52, v52, v112, v80
	s_nop 0
	v_max3_f32 v52, v52, v113, v81
	s_nop 0
	v_max3_f32 v52, v52, v114, v82
	s_nop 0
	v_max3_f32 v52, v52, v115, v83
	s_nop 0
	v_mov_b32_e32 v53, v52
	s_nop 1
	v_permlane32_swap_b32_e32 v52, v53
	v_max_f32_e32 v53, v53, v53
	v_max_f32_e32 v52, v52, v52
	v_max_f32_e32 v52, v52, v53
	v_cmp_lt_f32_e32 vcc, s13, v52
	s_cbranch_vccz .LBB0_1460
	v_max_f32_e32 v52, v52, v52
	v_max_f32_e32 v52, 0, v52
	v_exp_f32_e64 v53, -v52
	s_and_saveexec_b64 s[6:7], s[36:37]
	ds_write_b32 v170, v53
	s_or_b64 exec, exec, s[6:7]
	v_mul_f32_e32 v171, v171, v53
	s_waitcnt lgkmcnt(0)
	v_add_u32_e32 v53, s28, v169
	ds_read_b128 v[54:57], v53
	ds_read_b128 v[58:61], v53 offset:32
	ds_read_b128 v[62:65], v53 offset:64
	ds_read_b128 v[84:87], v53 offset:96
	s_waitcnt lgkmcnt(0)
	s_waitcnt lgkmcnt(3)
	v_pk_mul_f32 v[6:7], v[6:7], v[56:57]
	s_waitcnt lgkmcnt(2)
	v_pk_mul_f32 v[8:9], v[8:9], v[58:59]
	s_waitcnt lgkmcnt(1)
	v_pk_mul_f32 v[12:13], v[12:13], v[62:63]
	s_waitcnt lgkmcnt(0)
	v_pk_mul_f32 v[16:17], v[16:17], v[84:85]
	v_pk_mul_f32 v[18:19], v[18:19], v[86:87]
	v_pk_mul_f32 v[14:15], v[14:15], v[64:65]
	v_pk_mul_f32 v[10:11], v[10:11], v[60:61]
	v_pk_mul_f32 v[4:5], v[4:5], v[54:55]
	v_pk_mul_f32 v[32:33], v[32:33], v[84:85]
	v_pk_mul_f32 v[28:29], v[28:29], v[62:63]
	v_pk_mul_f32 v[24:25], v[24:25], v[58:59]
	v_pk_mul_f32 v[34:35], v[34:35], v[86:87]
	v_pk_mul_f32 v[30:31], v[30:31], v[64:65]
	v_pk_mul_f32 v[26:27], v[26:27], v[60:61]
	v_pk_mul_f32 v[22:23], v[22:23], v[56:57]
	v_pk_mul_f32 v[20:21], v[20:21], v[54:55]
	v_sub_f32_e32 v115, v115, v52
	v_sub_f32_e32 v114, v114, v52
	v_sub_f32_e32 v113, v113, v52
	v_sub_f32_e32 v112, v112, v52
	v_sub_f32_e32 v111, v111, v52
	v_sub_f32_e32 v110, v110, v52
	v_sub_f32_e32 v109, v109, v52
	v_sub_f32_e32 v108, v108, v52
	v_sub_f32_e32 v107, v107, v52
	v_sub_f32_e32 v106, v106, v52
	v_sub_f32_e32 v105, v105, v52
	v_sub_f32_e32 v104, v104, v52
	v_sub_f32_e32 v103, v103, v52
	v_sub_f32_e32 v102, v102, v52
	v_sub_f32_e32 v101, v101, v52
	v_sub_f32_e32 v100, v100, v52
	v_sub_f32_e32 v83, v83, v52
	v_sub_f32_e32 v82, v82, v52
	v_sub_f32_e32 v81, v81, v52
	v_sub_f32_e32 v80, v80, v52
	v_sub_f32_e32 v79, v79, v52
	v_sub_f32_e32 v78, v78, v52
	v_sub_f32_e32 v77, v77, v52
	v_sub_f32_e32 v76, v76, v52
	v_sub_f32_e32 v75, v75, v52
	v_sub_f32_e32 v74, v74, v52
	v_sub_f32_e32 v73, v73, v52
	v_sub_f32_e32 v72, v72, v52
	v_sub_f32_e32 v71, v71, v52
	v_sub_f32_e32 v70, v70, v52
	v_sub_f32_e32 v69, v69, v52
	v_sub_f32_e32 v68, v68, v52
	v_sub_f32_e32 v51, v51, v52
	v_sub_f32_e32 v50, v50, v52
	v_sub_f32_e32 v49, v49, v52
	v_sub_f32_e32 v48, v48, v52
	v_sub_f32_e32 v47, v47, v52
	v_sub_f32_e32 v46, v46, v52
	v_sub_f32_e32 v45, v45, v52
	v_sub_f32_e32 v44, v44, v52
	v_sub_f32_e32 v43, v43, v52
	v_sub_f32_e32 v42, v42, v52
	v_sub_f32_e32 v41, v41, v52
	v_sub_f32_e32 v40, v40, v52
	v_sub_f32_e32 v39, v39, v52
	v_sub_f32_e32 v38, v38, v52
	v_sub_f32_e32 v37, v37, v52
	v_sub_f32_e32 v36, v36, v52

.LBB0_1464:
	s_add_i32 s79, s79, 2
	s_and_b32 s2, s79, 2
	s_mulk_i32 s2, 0x3000
	v_add_u32_e32 v56, s2, v168
	ds_read_b128 v[52:55], v56
	ds_read_b128 v[172:175], v56 offset:512
	ds_read_b128 v[176:179], v56 offset:2048
	ds_read_b128 v[180:183], v56 offset:2560
	ds_read_b128 v[184:187], v56 offset:4096
	ds_read_b128 v[190:193], v56 offset:4608
	ds_read_b128 v[212:215], v56 offset:6144
	ds_read_b128 v[216:219], v56 offset:6656
	ds_read_b128 v[224:227], v56 offset:8192
	ds_read_b128 v[228:231], v56 offset:8704
	ds_read_b128 v[232:235], v56 offset:10240
	ds_read_b128 v[236:239], v56 offset:10752
	s_waitcnt lgkmcnt(11)
	v_mfma_f32_32x32x16_bf16 v[84:99], v[52:55], v[116:119], v[36:51]
	v_exp_f32_e32 v100, v100
	v_exp_f32_e32 v101, v101
	v_exp_f32_e32 v102, v102
	v_exp_f32_e32 v103, v103
	s_waitcnt lgkmcnt(10)
	v_mfma_f32_32x32x16_bf16 v[52:67], v[172:175], v[116:119], v[36:51]
	v_add_f32_e64 v172, v100, 0
	v_add_f32_e64 v173, v101, 0
	v_add_f32_e64 v172, v102, v172
	v_add_f32_e64 v173, v103, v173
	s_waitcnt lgkmcnt(9)
	v_mfma_f32_32x32x16_bf16 v[84:99], v[176:179], v[120:123], v[84:99]
	v_exp_f32_e32 v104, v104
	v_exp_f32_e32 v105, v105
	v_exp_f32_e32 v106, v106
	v_exp_f32_e32 v107, v107
	v_pk_add_f32 v[172:173], v[104:105], v[172:173]
	s_nop 0
	v_pk_add_f32 v[172:173], v[106:107], v[172:173]
	s_waitcnt lgkmcnt(8)
	v_mfma_f32_32x32x16_bf16 v[52:67], v[180:183], v[120:123], v[52:67]
	s_waitcnt lgkmcnt(7)
	v_mfma_f32_32x32x16_bf16 v[84:99], v[184:187], v[124:127], v[84:99]
	v_exp_f32_e32 v108, v108
	v_exp_f32_e32 v109, v109
	v_exp_f32_e32 v110, v110
	v_exp_f32_e32 v111, v111
	v_pk_add_f32 v[172:173], v[108:109], v[172:173]
	s_nop 0
	v_pk_add_f32 v[172:173], v[110:111], v[172:173]
	s_waitcnt lgkmcnt(6)
	v_mfma_f32_32x32x16_bf16 v[52:67], v[190:193], v[124:127], v[52:67]
	s_waitcnt lgkmcnt(5)
	v_mfma_f32_32x32x16_bf16 v[84:99], v[212:215], v[128:131], v[84:99]
	v_exp_f32_e32 v112, v112
	v_exp_f32_e32 v113, v113
	v_exp_f32_e32 v114, v114
	v_exp_f32_e32 v115, v115
	v_pk_add_f32 v[172:173], v[112:113], v[172:173]
	s_nop 0
	v_pk_add_f32 v[172:173], v[114:115], v[172:173]
	s_waitcnt lgkmcnt(4)
	v_mfma_f32_32x32x16_bf16 v[52:67], v[216:219], v[128:131], v[52:67]
	v_exp_f32_e32 v174, v68
	v_exp_f32_e32 v175, v69
	s_waitcnt lgkmcnt(3)
	v_mfma_f32_32x32x16_bf16 v[84:99], v[224:227], v[132:135], v[84:99]
	v_add_f32_e64 v68, v174, v172
	v_add_f32_e64 v69, v175, v173
	v_exp_f32_e32 v172, v70
	v_exp_f32_e32 v173, v71
	s_nop 0
	v_pk_add_f32 v[68:69], v[172:173], v[68:69]
	s_waitcnt lgkmcnt(2)
	v_mfma_f32_32x32x16_bf16 v[52:67], v[228:231], v[132:135], v[52:67]
	s_waitcnt lgkmcnt(1)
	v_mfma_f32_32x32x16_bf16 v[84:99], v[232:235], v[136:139], v[84:99]
	v_exp_f32_e32 v176, v72
	v_exp_f32_e32 v177, v73
	v_exp_f32_e32 v178, v74
	v_exp_f32_e32 v179, v75
	v_pk_add_f32 v[68:69], v[176:177], v[68:69]
	s_nop 0
	v_pk_add_f32 v[194:195], v[178:179], v[68:69]
	s_waitcnt lgkmcnt(0)
	v_mfma_f32_32x32x16_bf16 v[52:67], v[236:239], v[136:139], v[52:67]
	s_add_i32 s2, s78, 0x2000
	s_and_b32 s2, s2, 0x6000
	v_add_u32_e32 v212, s2, v2
	v_cvt_pk_bf16_f32 v70, v104, v105
	ds_read_b64_tr_b16 v[104:105],v212 offset:0
	v_cvt_pk_bf16_f32 v71, v106, v107
	ds_read_b64_tr_b16 v[106:107],v212 offset:512
	v_cvt_pk_bf16_f32 v69, v102, v103
	v_cvt_pk_bf16_f32 v102, v176, v177
	ds_read_b64_tr_b16 v[176:177],v212 offset:4096
	v_cvt_pk_bf16_f32 v103, v178, v179
	ds_read_b64_tr_b16 v[178:179],v212 offset:4608
	v_cvt_pk_bf16_f32 v72, v108, v109
	ds_read_b64_tr_b16 v[108:109],v212 offset:1024
	v_cvt_pk_bf16_f32 v73, v110, v111
	ds_read_b64_tr_b16 v[110:111],v212 offset:1536
	ds_read_b64_tr_b16 v[180:181],v212 offset:5120
	ds_read_b64_tr_b16 v[182:183],v212 offset:5632
	v_cvt_pk_bf16_f32 v74, v112, v113
	ds_read_b64_tr_b16 v[112:113],v212 offset:2048
	v_cvt_pk_bf16_f32 v75, v114, v115
	ds_read_b64_tr_b16 v[114:115],v212 offset:2560
	ds_read_b64_tr_b16 v[184:185],v212 offset:6144
	ds_read_b64_tr_b16 v[186:187],v212 offset:6656
	v_cvt_pk_bf16_f32 v68, v100, v101
	v_cvt_pk_bf16_f32 v101, v172, v173
	ds_read_b64_tr_b16 v[172:173],v212 offset:3072
	v_cvt_pk_bf16_f32 v100, v174, v175
	ds_read_b64_tr_b16 v[174:175],v212 offset:3584
	ds_read_b64_tr_b16 v[190:191],v212 offset:7168
	ds_read_b64_tr_b16 v[192:193],v212 offset:7680
	s_waitcnt lgkmcnt(14)
	v_mfma_f32_32x32x16_bf16 v[4:19], v[68:71], v[104:107], v[4:19]
	s_waitcnt lgkmcnt(12)
	v_mfma_f32_32x32x16_bf16 v[20:35], v[68:71], v[176:179], v[20:35]
	v_exp_f32_e32 v68, v76
	v_exp_f32_e32 v69, v77
	v_exp_f32_e32 v76, v78
	v_exp_f32_e32 v77, v79
	v_pk_add_f32 v[70:71], v[68:69], v[194:195]
	s_nop 0
	v_pk_add_f32 v[70:71], v[76:77], v[70:71]
	s_waitcnt lgkmcnt(10)
	v_mfma_f32_32x32x16_bf16 v[4:19], v[72:75], v[108:111], v[4:19]
	v_cvt_pk_bf16_f32 v68, v68, v69
	v_cvt_pk_bf16_f32 v69, v76, v77
	s_waitcnt lgkmcnt(8)
	v_mfma_f32_32x32x16_bf16 v[20:35], v[72:75], v[180:183], v[20:35]
	v_exp_f32_e32 v72, v80
	v_exp_f32_e32 v73, v81
	v_exp_f32_e32 v74, v82
	v_exp_f32_e32 v75, v83
	v_pk_add_f32 v[70:71], v[72:73], v[70:71]
	s_nop 0
	v_pk_add_f32 v[78:79], v[74:75], v[70:71]
	v_cvt_pk_bf16_f32 v70, v72, v73
	v_add_f32_e32 v72, v78, v79
	v_add_f32_e32 v171, v171, v72
	v_cvt_pk_bf16_f32 v71, v74, v75
	s_waitcnt lgkmcnt(6)
	v_mfma_f32_32x32x16_bf16 v[4:19], v[100:103], v[112:115], v[4:19]
	v_max3_f32 v72, v84, v52, v85
	s_nop 0
	v_max3_f32 v72, v72, v53, v86
	s_nop 0
	v_max3_f32 v72, v72, v54, v87
	s_nop 0
	v_max3_f32 v72, v72, v55, v88
	s_waitcnt lgkmcnt(4)
	v_mfma_f32_32x32x16_bf16 v[20:35], v[100:103], v[184:187], v[20:35]
	v_max3_f32 v72, v72, v56, v89
	s_nop 0
	v_max3_f32 v72, v72, v57, v90
	s_nop 0
	v_max3_f32 v72, v72, v58, v91
	s_nop 0
	v_max3_f32 v72, v72, v59, v91
	s_waitcnt lgkmcnt(2)
	v_mfma_f32_32x32x16_bf16 v[4:19], v[68:71], v[172:175], v[4:19]
	s_waitcnt lgkmcnt(0)
	v_mfma_f32_32x32x16_bf16 v[20:35], v[68:71], v[190:193], v[20:35]
	v_max3_f32 v68, v72, v92, v60
	s_nop 0
	v_max3_f32 v68, v68, v93, v61
	s_nop 0
	v_max3_f32 v68, v68, v94, v62
	s_nop 0
	v_max3_f32 v68, v68, v95, v63
	s_nop 0
	v_max3_f32 v68, v68, v96, v64
	s_nop 0
	v_max3_f32 v68, v68, v97, v65
	s_nop 0
	v_max3_f32 v68, v68, v98, v66
	s_nop 0
	v_max3_f32 v68, v68, v99, v67
	s_nop 0
	v_mov_b32_e32 v69, v68
	s_nop 1
	v_permlane32_swap_b32_e32 v68, v69
	s_andn2_b64 vcc, exec, s[62:63]
	s_cbranch_vccnz .LBB0_1451
	v_max_f32_e32 v68, v68, v68
	v_max_f32_e32 v69, v69, v69
	v_max_f32_e32 v68, v68, v69
	v_cmp_lt_f32_e32 vcc, s13, v68
	s_cbranch_vccz .LBB0_1451
	v_max_f32_e32 v68, v68, v68
	v_max_f32_e32 v68, 0, v68
	v_exp_f32_e64 v69, -v68
	s_and_saveexec_b64 s[6:7], s[36:37]
	s_cbranch_execz .LBB0_1450
	ds_write_b32 v170, v69
	s_branch .LBB0_1450

.LBB0_1566:
	s_add_i32 s6, s60, 1
	s_and_b32 s2, s6, 3
	s_mulk_i32 s2, 0x3000
	v_add_u32_e32 v88, s2, v215
	ds_read_b128 v[84:87], v88
	ds_read_b128 v[116:119], v88 offset:512
	ds_read_b128 v[120:123], v88 offset:2048
	ds_read_b128 v[124:127], v88 offset:2560
	ds_read_b128 v[128:131], v88 offset:4096
	ds_read_b128 v[132:135], v88 offset:4608
	ds_read_b128 v[136:139], v88 offset:6144
	ds_read_b128 v[140:143], v88 offset:6656
	s_waitcnt lgkmcnt(7)
	v_mfma_f32_32x32x16_bf16 v[100:115], v[84:87], v[148:151], v[36:51]
	v_exp_f32_e32 v68, v68
	v_exp_f32_e32 v69, v69
	v_exp_f32_e32 v70, v70
	v_exp_f32_e32 v71, v71
	v_exp_f32_e32 v72, v72
	v_exp_f32_e32 v73, v73
	s_waitcnt lgkmcnt(6)
	v_mfma_f32_32x32x16_bf16 v[84:99], v[116:119], v[148:151], v[36:51]
	s_waitcnt lgkmcnt(5)
	v_mfma_f32_32x32x16_bf16 v[100:115], v[120:123], v[152:155], v[100:115]
	v_exp_f32_e32 v74, v74
	v_exp_f32_e32 v75, v75
	s_waitcnt lgkmcnt(4)
	v_mfma_f32_32x32x16_bf16 v[84:99], v[124:127], v[152:155], v[84:99]
	s_waitcnt lgkmcnt(3)
	v_mfma_f32_32x32x16_bf16 v[100:115], v[128:131], v[156:159], v[100:115]
	s_waitcnt lgkmcnt(2)
	v_mfma_f32_32x32x16_bf16 v[84:99], v[132:135], v[156:159], v[84:99]
	s_waitcnt lgkmcnt(1)
	v_mfma_f32_32x32x16_bf16 v[100:115], v[136:139], v[160:163], v[100:115]
	s_waitcnt lgkmcnt(0)
	v_mfma_f32_32x32x16_bf16 v[84:99], v[140:143], v[160:163], v[84:99]
	s_and_b32 s2, s57, 0x4000
	v_add_u32_e32 v128, s2, v217
	ds_read_b64_tr_b16 v[120:121],v128 offset:0
	ds_read_b64_tr_b16 v[122:123],v128 offset:512
	ds_read_b64_tr_b16 v[124:125],v128 offset:4096
	ds_read_b64_tr_b16 v[126:127],v128 offset:4608
	ds_read_b64_tr_b16 v[180:181],v128 offset:1024
	ds_read_b64_tr_b16 v[182:183],v128 offset:1536
	ds_read_b64_tr_b16 v[184:185],v128 offset:5120
	ds_read_b64_tr_b16 v[186:187],v128 offset:5632
	ds_read_b64_tr_b16 v[176:177],v128 offset:2048
	ds_read_b64_tr_b16 v[178:179],v128 offset:2560
	ds_read_b64_tr_b16 v[172:173],v128 offset:6144
	ds_read_b64_tr_b16 v[174:175],v128 offset:6656
	ds_read_b64_tr_b16 v[164:165],v128 offset:3072
	ds_read_b64_tr_b16 v[166:167],v128 offset:3584
	ds_read_b64_tr_b16 v[168:169],v128 offset:7168
	ds_read_b64_tr_b16 v[170:171],v128 offset:7680
	v_cvt_pk_bf16_f32 v116, v68, v69
	v_cvt_pk_bf16_f32 v117, v70, v71
	v_cvt_pk_bf16_f32 v118, v72, v73
	v_cvt_pk_bf16_f32 v119, v74, v75
	s_nop 1
	s_waitcnt lgkmcnt(14)
	v_mfma_f32_32x32x16_bf16 v[4:19], v[116:119], v[120:123], v[4:19]
	s_cmp_ge_i32 s6, s25
	s_waitcnt lgkmcnt(12)
	v_mfma_f32_32x32x16_bf16 v[20:35], v[116:119], v[124:127], v[20:35]
	s_cbranch_scc1 .LBB0_1576
	s_add_i32 s2, s56, s58
	s_add_i32 s3, s2, 0xffffffa0
	s_cmp_gt_u32 s3, 0xfffffea0
	s_cbranch_scc0 .LBB0_1572
	s_add_i32 s2, s2, -2
	s_cmp_lt_u32 s2, 0xffffff5d
	s_mov_b64 s[50:51], 0
	s_cbranch_scc0 .LBB0_1592
	v_add_u32_e32 v130, s56, v218
	v_add_u32_e32 v116, 0xffffffbf, v130
	v_cmp_lt_u32_e32 vcc, s14, v116
	v_subrev_u32_e32 v116, 33, v130
	v_subrev_u32_e32 v117, 64, v130
	v_cndmask_b32_e32 v100, v210, v100, vcc
	v_cmp_lt_u32_e32 vcc, s14, v116
	v_subrev_u32_e32 v118, 63, v130
	v_subrev_u32_e32 v119, 62, v130
	v_cndmask_b32_e32 v116, v210, v84, vcc
	v_cmp_lt_u32_e32 vcc, s14, v117
	v_subrev_u32_e32 v117, 32, v130
	v_subrev_u32_e32 v120, 57, v130
	v_cndmask_b32_e32 v101, v210, v101, vcc
	v_cmp_lt_u32_e32 vcc, s14, v117
	v_subrev_u32_e32 v121, 56, v130
	v_subrev_u32_e32 v122, 55, v130
	v_cndmask_b32_e32 v117, v210, v85, vcc
	v_cmp_lt_u32_e32 vcc, s14, v118
	v_subrev_u32_e32 v118, 31, v130
	v_subrev_u32_e32 v123, 54, v130
	v_cndmask_b32_e32 v102, v210, v102, vcc
	v_cmp_lt_u32_e32 vcc, s14, v118
	v_subrev_u32_e32 v124, 49, v130
	v_subrev_u32_e32 v125, 48, v130
	v_cndmask_b32_e32 v118, v210, v86, vcc
	v_cmp_lt_u32_e32 vcc, s14, v119
	v_subrev_u32_e32 v119, 30, v130
	v_subrev_u32_e32 v126, 47, v130
	v_cndmask_b32_e32 v103, v210, v103, vcc
	v_cmp_lt_u32_e32 vcc, s14, v119
	v_subrev_u32_e32 v127, 46, v130
	v_subrev_u32_e32 v128, 41, v130
	v_cndmask_b32_e32 v119, v210, v87, vcc
	v_cmp_lt_u32_e32 vcc, s14, v120
	v_subrev_u32_e32 v120, 25, v130
	v_subrev_u32_e32 v129, 40, v130
	v_cndmask_b32_e32 v104, v210, v104, vcc
	v_cmp_lt_u32_e32 vcc, s14, v120
	v_subrev_u32_e32 v131, 39, v130
	s_mov_b64 s[52:53], -1
	v_cndmask_b32_e32 v120, v210, v88, vcc
	v_cmp_lt_u32_e32 vcc, s14, v121
	v_subrev_u32_e32 v121, 24, v130
	s_nop 0
	v_cndmask_b32_e32 v105, v210, v105, vcc
	v_cmp_lt_u32_e32 vcc, s14, v121
	s_nop 1
	v_cndmask_b32_e32 v121, v210, v89, vcc
	v_cmp_lt_u32_e32 vcc, s14, v122
	v_subrev_u32_e32 v122, 23, v130
	s_nop 0
	v_cndmask_b32_e32 v106, v210, v106, vcc
	v_cmp_lt_u32_e32 vcc, s14, v122
	s_nop 1
	v_cndmask_b32_e32 v122, v210, v90, vcc
	v_cmp_lt_u32_e32 vcc, s14, v123
	v_subrev_u32_e32 v123, 22, v130
	s_nop 0
	v_cndmask_b32_e32 v107, v210, v107, vcc
	v_cmp_lt_u32_e32 vcc, s14, v123
	s_nop 1
	v_cndmask_b32_e32 v123, v210, v91, vcc
	v_cmp_lt_u32_e32 vcc, s14, v124
	v_subrev_u32_e32 v124, 17, v130
	s_nop 0
	v_cndmask_b32_e32 v108, v210, v108, vcc
	v_cmp_lt_u32_e32 vcc, s14, v124
	s_nop 1
	v_cndmask_b32_e32 v124, v210, v92, vcc
	v_cmp_lt_u32_e32 vcc, s14, v125
	v_add_u32_e32 v125, -16, v130
	s_nop 0
	v_cndmask_b32_e32 v109, v210, v109, vcc
	v_cmp_lt_u32_e32 vcc, s14, v125
	s_nop 1
	v_cndmask_b32_e32 v125, v210, v93, vcc
	v_cmp_lt_u32_e32 vcc, s14, v126
	v_add_u32_e32 v126, -15, v130
	s_nop 0
	v_cndmask_b32_e32 v110, v210, v110, vcc
	v_cmp_lt_u32_e32 vcc, s14, v126
	s_nop 1
	v_cndmask_b32_e32 v126, v210, v94, vcc
	v_cmp_lt_u32_e32 vcc, s14, v127
	v_add_u32_e32 v127, -14, v130
	s_nop 0
	v_cndmask_b32_e32 v111, v210, v111, vcc
	v_cmp_lt_u32_e32 vcc, s14, v127
	s_nop 1
	v_cndmask_b32_e32 v127, v210, v95, vcc
	v_cmp_lt_u32_e32 vcc, s14, v128
	v_add_u32_e32 v128, -9, v130
	s_nop 0
	v_cndmask_b32_e32 v112, v210, v112, vcc
	v_cmp_lt_u32_e32 vcc, s14, v128
	s_nop 1
	v_cndmask_b32_e32 v128, v210, v96, vcc
	v_cmp_lt_u32_e32 vcc, s14, v129
	v_add_u32_e32 v129, -8, v130
	s_nop 0
	v_cndmask_b32_e32 v113, v210, v113, vcc
	v_cmp_lt_u32_e32 vcc, s14, v129
	s_nop 1
	v_cndmask_b32_e32 v129, v210, v97, vcc
	v_cmp_lt_u32_e32 vcc, s14, v131
	v_add_u32_e32 v131, -7, v130
	s_nop 0
	v_cndmask_b32_e32 v114, v210, v114, vcc
	v_cmp_lt_u32_e32 vcc, s14, v131
	v_subrev_u32_e32 v131, 38, v130
	v_add_u32_e32 v130, -6, v130
	v_cndmask_b32_e32 v132, v210, v98, vcc
	v_cmp_lt_u32_e32 vcc, s14, v131
	s_nop 1
	v_cndmask_b32_e32 v115, v210, v115, vcc
	v_cmp_lt_u32_e32 vcc, s14, v130
	s_nop 1
	v_cndmask_b32_e32 v131, v210, v99, vcc
	s_and_b64 vcc, exec, s[50:51]
	s_cbranch_vccnz .LBB0_1573
	s_branch .LBB0_1574

.LBB0_1576:
	v_pk_add_f32 v[116:117], v[68:69], 0 op_sel_hi:[1,0]
	v_exp_f32_e32 v76, v76
	v_exp_f32_e32 v77, v77
	v_pk_add_f32 v[116:117], v[70:71], v[116:117]
	v_exp_f32_e32 v78, v78
	v_exp_f32_e32 v79, v79
	v_pk_add_f32 v[116:117], v[72:73], v[116:117]
	v_exp_f32_e32 v80, v80
	v_exp_f32_e32 v81, v81
	v_pk_add_f32 v[116:117], v[74:75], v[116:117]
	v_exp_f32_e32 v82, v82
	v_exp_f32_e32 v83, v83
	v_pk_add_f32 v[116:117], v[76:77], v[116:117]
	v_exp_f32_e32 v52, v52
	v_exp_f32_e32 v53, v53
	v_pk_add_f32 v[116:117], v[78:79], v[116:117]
	v_exp_f32_e32 v54, v54
	v_exp_f32_e32 v55, v55
	v_pk_add_f32 v[116:117], v[80:81], v[116:117]
	v_exp_f32_e32 v56, v56
	v_exp_f32_e32 v57, v57
	v_pk_add_f32 v[116:117], v[82:83], v[116:117]
	v_exp_f32_e32 v58, v58
	v_exp_f32_e32 v59, v59
	v_pk_add_f32 v[116:117], v[52:53], v[116:117]
	v_exp_f32_e32 v60, v60
	v_exp_f32_e32 v61, v61
	v_pk_add_f32 v[116:117], v[54:55], v[116:117]
	v_exp_f32_e32 v62, v62
	v_exp_f32_e32 v63, v63
	v_pk_add_f32 v[116:117], v[56:57], v[116:117]
	v_cvt_pk_bf16_f32 v118, v80, v81
	v_pk_add_f32 v[124:125], v[58:59], v[116:117]
	v_cvt_pk_bf16_f32 v116, v76, v77
	v_cvt_pk_bf16_f32 v117, v78, v79
	v_pk_add_f32 v[124:125], v[60:61], v[124:125]
	v_cvt_pk_bf16_f32 v119, v82, v83
	v_cvt_pk_bf16_f32 v120, v52, v53
	v_cvt_pk_bf16_f32 v121, v54, v55
	v_cvt_pk_bf16_f32 v122, v56, v57
	v_cvt_pk_bf16_f32 v123, v58, v59
	v_pk_add_f32 v[124:125], v[62:63], v[124:125]
	s_waitcnt lgkmcnt(10)
	v_mfma_f32_32x32x16_bf16 v[4:19], v[116:119], v[180:183], v[4:19]
	v_exp_f32_e32 v64, v64
	v_exp_f32_e32 v65, v65
	v_exp_f32_e32 v66, v66
	v_exp_f32_e32 v67, v67
	s_waitcnt lgkmcnt(8)
	v_mfma_f32_32x32x16_bf16 v[20:35], v[116:119], v[184:187], v[20:35]
	v_add_f32_e64 v116, v64, v124
	v_add_f32_e64 v117, v65, v125
	v_cvt_pk_bf16_f32 v118, v64, v65
	v_add_f32_e64 v124, v66, v116
	v_add_f32_e64 v125, v67, v117
	v_cvt_pk_bf16_f32 v116, v60, v61
	v_add_f32_e32 v124, v124, v125
	v_cvt_pk_bf16_f32 v117, v62, v63
	v_add_f32_e32 v216, v216, v124
	v_cvt_pk_bf16_f32 v119, v66, v67
	s_waitcnt lgkmcnt(6)
	v_mfma_f32_32x32x16_bf16 v[4:19], v[120:123], v[176:179], v[4:19]
	v_max3_f32 v124, v100, v84, v101
	s_nop 0
	v_max3_f32 v124, v124, v85, v102
	s_nop 0
	v_max3_f32 v124, v124, v86, v103
	s_nop 0
	v_max3_f32 v124, v124, v87, v104
	s_waitcnt lgkmcnt(4)
	v_mfma_f32_32x32x16_bf16 v[20:35], v[120:123], v[172:175], v[20:35]
	v_max3_f32 v124, v124, v88, v105
	s_nop 0
	v_max3_f32 v124, v124, v89, v106
	s_nop 0
	v_max3_f32 v124, v124, v90, v107
	s_nop 0
	v_max3_f32 v124, v124, v91, v107
	s_waitcnt lgkmcnt(2)
	v_mfma_f32_32x32x16_bf16 v[4:19], v[116:119], v[164:167], v[4:19]
	s_waitcnt lgkmcnt(0)
	v_mfma_f32_32x32x16_bf16 v[20:35], v[116:119], v[168:171], v[20:35]
	v_max3_f32 v116, v124, v108, v92
	s_nop 0
	v_max3_f32 v116, v116, v109, v93
	s_nop 0
	v_max3_f32 v116, v116, v110, v94
	s_nop 0
	v_max3_f32 v116, v116, v111, v95
	s_nop 0
	v_max3_f32 v116, v116, v112, v96
	s_nop 0
	v_max3_f32 v116, v116, v113, v97
	s_nop 0
	v_max3_f32 v116, v116, v114, v98
	s_nop 0
	v_max3_f32 v116, v116, v115, v99
	s_nop 0
	v_mov_b32_e32 v117, v116
	s_nop 1
	v_permlane32_swap_b32_e32 v116, v117
	s_cmp_lt_i32 s6, s54
	s_cselect_b64 s[50:51], -1, 0
	s_cmp_ge_i32 s6, s54
	s_cbranch_scc1 .LBB0_1581
	v_max_f32_e32 v116, v116, v116
	v_max_f32_e32 v117, v117, v117
	v_max_f32_e32 v116, v116, v117
	v_cmp_lt_f32_e32 vcc, s13, v116
	s_cbranch_vccz .LBB0_1581
	v_max_f32_e32 v116, v116, v116
	v_max_f32_e32 v116, 0, v116
	v_exp_f32_e64 v117, -v116
	s_and_saveexec_b64 s[6:7], s[38:39]
	ds_write_b32 v2, v117
	s_or_b64 exec, exec, s[6:7]
	v_mul_f32_e32 v216, v216, v117
	s_waitcnt lgkmcnt(0)
	v_add_u32_e32 v117, s28, v190
	ds_read_b128 v[118:121], v117
	ds_read_b128 v[122:125], v117 offset:32
	ds_read_b128 v[126:129], v117 offset:64
	ds_read_b128 v[130:133], v117 offset:96
	s_waitcnt lgkmcnt(0)
	s_waitcnt lgkmcnt(3)
	v_pk_mul_f32 v[6:7], v[6:7], v[120:121]
	s_waitcnt lgkmcnt(2)
	v_pk_mul_f32 v[8:9], v[8:9], v[122:123]
	s_waitcnt lgkmcnt(1)
	v_pk_mul_f32 v[12:13], v[12:13], v[126:127]
	s_waitcnt lgkmcnt(0)
	v_pk_mul_f32 v[16:17], v[16:17], v[130:131]
	v_pk_mul_f32 v[18:19], v[18:19], v[132:133]
	v_pk_mul_f32 v[14:15], v[14:15], v[128:129]
	v_pk_mul_f32 v[10:11], v[10:11], v[124:125]
	v_pk_mul_f32 v[4:5], v[4:5], v[118:119]
	v_pk_mul_f32 v[32:33], v[32:33], v[130:131]
	v_pk_mul_f32 v[28:29], v[28:29], v[126:127]
	v_pk_mul_f32 v[24:25], v[24:25], v[122:123]
	v_pk_mul_f32 v[34:35], v[34:35], v[132:133]
	v_pk_mul_f32 v[30:31], v[30:31], v[128:129]
	v_pk_mul_f32 v[26:27], v[26:27], v[124:125]
	v_pk_mul_f32 v[22:23], v[22:23], v[120:121]
	v_pk_mul_f32 v[20:21], v[20:21], v[118:119]
	v_sub_f32_e32 v115, v115, v116
	v_sub_f32_e32 v114, v114, v116
	v_sub_f32_e32 v113, v113, v116
	v_sub_f32_e32 v112, v112, v116
	v_sub_f32_e32 v111, v111, v116
	v_sub_f32_e32 v110, v110, v116
	v_sub_f32_e32 v109, v109, v116
	v_sub_f32_e32 v108, v108, v116
	v_sub_f32_e32 v107, v107, v116
	v_sub_f32_e32 v106, v106, v116
	v_sub_f32_e32 v105, v105, v116
	v_sub_f32_e32 v104, v104, v116
	v_sub_f32_e32 v103, v103, v116
	v_sub_f32_e32 v102, v102, v116
	v_sub_f32_e32 v101, v101, v116
	v_sub_f32_e32 v100, v100, v116
	v_sub_f32_e32 v99, v99, v116
	v_sub_f32_e32 v98, v98, v116
	v_sub_f32_e32 v97, v97, v116
	v_sub_f32_e32 v96, v96, v116
	v_sub_f32_e32 v95, v95, v116
	v_sub_f32_e32 v94, v94, v116
	v_sub_f32_e32 v93, v93, v116
	v_sub_f32_e32 v92, v92, v116
	v_sub_f32_e32 v91, v91, v116
	v_sub_f32_e32 v90, v90, v116
	v_sub_f32_e32 v89, v89, v116
	v_sub_f32_e32 v88, v88, v116
	v_sub_f32_e32 v87, v87, v116
	v_sub_f32_e32 v86, v86, v116
	v_sub_f32_e32 v85, v85, v116
	v_sub_f32_e32 v84, v84, v116
	v_sub_f32_e32 v51, v51, v116
	v_sub_f32_e32 v50, v50, v116
	v_sub_f32_e32 v49, v49, v116
	v_sub_f32_e32 v48, v48, v116
	v_sub_f32_e32 v47, v47, v116
	v_sub_f32_e32 v46, v46, v116
	v_sub_f32_e32 v45, v45, v116
	v_sub_f32_e32 v44, v44, v116
	v_sub_f32_e32 v43, v43, v116
	v_sub_f32_e32 v42, v42, v116
	v_sub_f32_e32 v41, v41, v116
	v_sub_f32_e32 v40, v40, v116
	v_sub_f32_e32 v39, v39, v116
	v_sub_f32_e32 v38, v38, v116
	v_sub_f32_e32 v37, v37, v116
	v_sub_f32_e32 v36, v36, v116

.LBB0_1586:
	s_and_b32 s2, s59, 2
	s_mulk_i32 s2, 0x3000
	v_add_u32_e32 v56, s2, v215
	ds_read_b128 v[52:55], v56
	ds_read_b128 v[116:119], v56 offset:512
	ds_read_b128 v[120:123], v56 offset:2048
	ds_read_b128 v[124:127], v56 offset:2560
	ds_read_b128 v[128:131], v56 offset:4096
	ds_read_b128 v[132:135], v56 offset:4608
	ds_read_b128 v[136:139], v56 offset:6144
	ds_read_b128 v[140:143], v56 offset:6656
	s_waitcnt lgkmcnt(7)
	v_mfma_f32_32x32x16_bf16 v[68:83], v[52:55], v[148:151], v[36:51]
	v_exp_f32_e32 v180, v100
	v_exp_f32_e32 v181, v101
	v_exp_f32_e32 v182, v102
	v_exp_f32_e32 v183, v103
	v_exp_f32_e32 v184, v104
	v_exp_f32_e32 v185, v105
	s_waitcnt lgkmcnt(6)
	v_mfma_f32_32x32x16_bf16 v[52:67], v[116:119], v[148:151], v[36:51]
	s_waitcnt lgkmcnt(5)
	v_mfma_f32_32x32x16_bf16 v[68:83], v[120:123], v[152:155], v[68:83]
	v_exp_f32_e32 v186, v106
	v_exp_f32_e32 v187, v107
	s_waitcnt lgkmcnt(4)
	v_mfma_f32_32x32x16_bf16 v[52:67], v[124:127], v[152:155], v[52:67]
	s_waitcnt lgkmcnt(3)
	v_mfma_f32_32x32x16_bf16 v[68:83], v[128:131], v[156:159], v[68:83]
	s_waitcnt lgkmcnt(2)
	v_mfma_f32_32x32x16_bf16 v[52:67], v[132:135], v[156:159], v[52:67]
	s_waitcnt lgkmcnt(1)
	v_mfma_f32_32x32x16_bf16 v[68:83], v[136:139], v[160:163], v[68:83]
	s_waitcnt lgkmcnt(0)
	v_mfma_f32_32x32x16_bf16 v[52:67], v[140:143], v[160:163], v[52:67]
	s_add_i32 s2, s57, 0x2000
	s_and_b32 s2, s2, 0x6000
	v_add_u32_e32 v128, s2, v217
	ds_read_b64_tr_b16 v[120:121],v128 offset:0
	ds_read_b64_tr_b16 v[122:123],v128 offset:512
	ds_read_b64_tr_b16 v[124:125],v128 offset:4096
	ds_read_b64_tr_b16 v[126:127],v128 offset:4608
	ds_read_b64_tr_b16 v[172:173],v128 offset:1024
	ds_read_b64_tr_b16 v[174:175],v128 offset:1536
	ds_read_b64_tr_b16 v[176:177],v128 offset:5120
	ds_read_b64_tr_b16 v[178:179],v128 offset:5632
	ds_read_b64_tr_b16 v[168:169],v128 offset:2048
	ds_read_b64_tr_b16 v[170:171],v128 offset:2560
	ds_read_b64_tr_b16 v[164:165],v128 offset:6144
	ds_read_b64_tr_b16 v[166:167],v128 offset:6656
	ds_read_b64_tr_b16 v[100:101],v128 offset:3072
	ds_read_b64_tr_b16 v[102:103],v128 offset:3584
	ds_read_b64_tr_b16 v[104:105],v128 offset:7168
	ds_read_b64_tr_b16 v[106:107],v128 offset:7680
	v_cvt_pk_bf16_f32 v116, v180, v181
	v_cvt_pk_bf16_f32 v117, v182, v183
	v_cvt_pk_bf16_f32 v118, v184, v185
	v_cvt_pk_bf16_f32 v119, v186, v187
	s_nop 1
	s_waitcnt lgkmcnt(14)
	v_mfma_f32_32x32x16_bf16 v[4:19], v[116:119], v[120:123], v[4:19]
	s_cmp_ge_i32 s59, s25
	s_waitcnt lgkmcnt(12)
	v_mfma_f32_32x32x16_bf16 v[20:35], v[116:119], v[124:127], v[20:35]
	s_cbranch_scc1 .LBB0_1597
	s_add_i32 s2, s56, s58
	s_sub_i32 s3, s2, 32
	s_cmp_gt_u32 s3, 0xfffffea0
	s_cbranch_scc0 .LBB0_1593
	s_add_i32 s2, s2, 62
	s_cmp_lt_u32 s2, 0xffffff5d
	s_mov_b64 s[50:51], 0
	s_cbranch_scc0 .LBB0_1604
	v_add_u32_e32 v130, s56, v218
	v_add_u32_e32 v116, -1, v130
	v_cmp_lt_u32_e32 vcc, s14, v116
	v_add_u32_e32 v116, 31, v130
	v_add_u32_e32 v117, 32, v130
	v_cndmask_b32_e32 v68, v210, v68, vcc
	v_cmp_lt_u32_e32 vcc, s14, v116
	v_add_u32_e32 v118, 1, v130
	v_add_u32_e32 v119, 2, v130
	v_cndmask_b32_e32 v116, v210, v52, vcc
	v_cmp_lt_u32_e32 vcc, s14, v130
	v_add_u32_e32 v120, 7, v130
	v_add_u32_e32 v121, 8, v130
	v_cndmask_b32_e32 v69, v210, v69, vcc
	v_cmp_lt_u32_e32 vcc, s14, v117
	v_add_u32_e32 v122, 9, v130
	v_add_u32_e32 v123, 10, v130
	v_cndmask_b32_e32 v117, v210, v53, vcc
	v_cmp_lt_u32_e32 vcc, s14, v118
	v_add_u32_e32 v118, 33, v130
	v_add_u32_e32 v124, 15, v130
	v_cndmask_b32_e32 v70, v210, v70, vcc
	v_cmp_lt_u32_e32 vcc, s14, v118
	v_add_u32_e32 v125, 16, v130
	v_add_u32_e32 v126, 17, v130
	v_cndmask_b32_e32 v118, v210, v54, vcc
	v_cmp_lt_u32_e32 vcc, s14, v119
	v_add_u32_e32 v119, 34, v130
	v_add_u32_e32 v127, 18, v130
	v_cndmask_b32_e32 v71, v210, v71, vcc
	v_cmp_lt_u32_e32 vcc, s14, v119
	v_add_u32_e32 v128, 23, v130
	v_add_u32_e32 v129, 24, v130
	v_cndmask_b32_e32 v119, v210, v55, vcc
	v_cmp_lt_u32_e32 vcc, s14, v120
	v_add_u32_e32 v120, 39, v130
	v_add_u32_e32 v131, 25, v130
	v_cndmask_b32_e32 v72, v210, v72, vcc
	v_cmp_lt_u32_e32 vcc, s14, v120
	s_mov_b64 s[52:53], -1
	s_nop 0
	v_cndmask_b32_e32 v120, v210, v56, vcc
	v_cmp_lt_u32_e32 vcc, s14, v121
	v_add_u32_e32 v121, 40, v130
	s_nop 0
	v_cndmask_b32_e32 v73, v210, v73, vcc
	v_cmp_lt_u32_e32 vcc, s14, v121
	s_nop 1
	v_cndmask_b32_e32 v121, v210, v57, vcc
	v_cmp_lt_u32_e32 vcc, s14, v122
	v_add_u32_e32 v122, 41, v130
	s_nop 0
	v_cndmask_b32_e32 v74, v210, v74, vcc
	v_cmp_lt_u32_e32 vcc, s14, v122
	s_nop 1
	v_cndmask_b32_e32 v122, v210, v58, vcc
	v_cmp_lt_u32_e32 vcc, s14, v123
	v_add_u32_e32 v123, 42, v130
	s_nop 0
	v_cndmask_b32_e32 v75, v210, v75, vcc
	v_cmp_lt_u32_e32 vcc, s14, v123
	s_nop 1
	v_cndmask_b32_e32 v123, v210, v59, vcc
	v_cmp_lt_u32_e32 vcc, s14, v124
	v_add_u32_e32 v124, 47, v130
	s_nop 0
	v_cndmask_b32_e32 v76, v210, v76, vcc
	v_cmp_lt_u32_e32 vcc, s14, v124
	s_nop 1
	v_cndmask_b32_e32 v124, v210, v60, vcc
	v_cmp_lt_u32_e32 vcc, s14, v125
	v_add_u32_e32 v125, 48, v130
	s_nop 0
	v_cndmask_b32_e32 v77, v210, v77, vcc
	v_cmp_lt_u32_e32 vcc, s14, v125
	s_nop 1
	v_cndmask_b32_e32 v125, v210, v61, vcc
	v_cmp_lt_u32_e32 vcc, s14, v126
	v_add_u32_e32 v126, 49, v130
	s_nop 0
	v_cndmask_b32_e32 v78, v210, v78, vcc
	v_cmp_lt_u32_e32 vcc, s14, v126
	s_nop 1
	v_cndmask_b32_e32 v126, v210, v62, vcc
	v_cmp_lt_u32_e32 vcc, s14, v127
	v_add_u32_e32 v127, 50, v130
	s_nop 0
	v_cndmask_b32_e32 v79, v210, v79, vcc
	v_cmp_lt_u32_e32 vcc, s14, v127
	s_nop 1
	v_cndmask_b32_e32 v127, v210, v63, vcc
	v_cmp_lt_u32_e32 vcc, s14, v128
	v_add_u32_e32 v128, 55, v130
	s_nop 0
	v_cndmask_b32_e32 v80, v210, v80, vcc
	v_cmp_lt_u32_e32 vcc, s14, v128
	s_nop 1
	v_cndmask_b32_e32 v128, v210, v64, vcc
	v_cmp_lt_u32_e32 vcc, s14, v129
	v_add_u32_e32 v129, 56, v130
	s_nop 0
	v_cndmask_b32_e32 v81, v210, v81, vcc
	v_cmp_lt_u32_e32 vcc, s14, v129
	s_nop 1
	v_cndmask_b32_e32 v129, v210, v65, vcc
	v_cmp_lt_u32_e32 vcc, s14, v131
	v_add_u32_e32 v131, 57, v130
	s_nop 0
	v_cndmask_b32_e32 v82, v210, v82, vcc
	v_cmp_lt_u32_e32 vcc, s14, v131
	v_add_u32_e32 v131, 26, v130
	v_add_u32_e32 v130, 58, v130
	v_cndmask_b32_e32 v132, v210, v66, vcc
	v_cmp_lt_u32_e32 vcc, s14, v131
	s_nop 1
	v_cndmask_b32_e32 v83, v210, v83, vcc
	v_cmp_lt_u32_e32 vcc, s14, v130
	s_nop 1
	v_cndmask_b32_e32 v131, v210, v67, vcc
	s_and_b64 vcc, exec, s[50:51]
	s_cbranch_vccnz .LBB0_1594
	s_branch .LBB0_1595

.LBB0_1597:
	v_pk_add_f32 v[116:117], v[180:181], 0 op_sel_hi:[1,0]
	v_exp_f32_e32 v108, v108
	v_exp_f32_e32 v109, v109
	v_pk_add_f32 v[116:117], v[182:183], v[116:117]
	v_exp_f32_e32 v110, v110
	v_exp_f32_e32 v111, v111
	v_pk_add_f32 v[116:117], v[184:185], v[116:117]
	v_exp_f32_e32 v112, v112
	v_exp_f32_e32 v113, v113
	v_pk_add_f32 v[116:117], v[186:187], v[116:117]
	v_exp_f32_e32 v114, v114
	v_exp_f32_e32 v115, v115
	v_pk_add_f32 v[116:117], v[108:109], v[116:117]
	v_exp_f32_e32 v118, v84
	v_exp_f32_e32 v119, v85
	v_pk_add_f32 v[116:117], v[110:111], v[116:117]
	v_exp_f32_e32 v120, v86
	v_exp_f32_e32 v121, v87
	v_pk_add_f32 v[116:117], v[112:113], v[116:117]
	v_exp_f32_e32 v122, v88
	v_exp_f32_e32 v123, v89
	v_pk_add_f32 v[116:117], v[114:115], v[116:117]
	v_exp_f32_e32 v124, v90
	v_exp_f32_e32 v125, v91
	v_pk_add_f32 v[84:85], v[118:119], v[116:117]
	v_exp_f32_e32 v92, v92
	v_exp_f32_e32 v93, v93
	v_pk_add_f32 v[84:85], v[120:121], v[84:85]
	v_exp_f32_e32 v94, v94
	v_exp_f32_e32 v95, v95
	v_pk_add_f32 v[84:85], v[122:123], v[84:85]
	v_cvt_pk_bf16_f32 v86, v112, v113
	v_pk_add_f32 v[116:117], v[124:125], v[84:85]
	v_cvt_pk_bf16_f32 v84, v108, v109
	v_cvt_pk_bf16_f32 v85, v110, v111
	v_pk_add_f32 v[108:109], v[92:93], v[116:117]
	v_cvt_pk_bf16_f32 v87, v114, v115
	v_cvt_pk_bf16_f32 v88, v118, v119
	v_cvt_pk_bf16_f32 v89, v120, v121
	v_cvt_pk_bf16_f32 v90, v122, v123
	v_cvt_pk_bf16_f32 v91, v124, v125
	v_pk_add_f32 v[108:109], v[94:95], v[108:109]
	s_waitcnt lgkmcnt(10)
	v_mfma_f32_32x32x16_bf16 v[4:19], v[84:87], v[172:175], v[4:19]
	s_waitcnt lgkmcnt(8)
	v_mfma_f32_32x32x16_bf16 v[20:35], v[84:87], v[176:179], v[20:35]
	v_exp_f32_e32 v86, v96
	v_exp_f32_e32 v87, v97
	v_exp_f32_e32 v96, v98
	v_exp_f32_e32 v97, v99
	v_pk_add_f32 v[84:85], v[86:87], v[108:109]
	v_cvt_pk_bf16_f32 v86, v86, v87
	v_pk_add_f32 v[98:99], v[96:97], v[84:85]
	v_cvt_pk_bf16_f32 v84, v92, v93
	v_add_f32_e32 v92, v98, v99
	v_cvt_pk_bf16_f32 v85, v94, v95
	v_add_f32_e32 v216, v216, v92
	v_cvt_pk_bf16_f32 v87, v96, v97
	s_waitcnt lgkmcnt(6)
	v_mfma_f32_32x32x16_bf16 v[4:19], v[88:91], v[168:171], v[4:19]
	v_max3_f32 v92, v68, v52, v69
	s_nop 0
	v_max3_f32 v92, v92, v53, v70
	s_nop 0
	v_max3_f32 v92, v92, v54, v71
	s_nop 0
	v_max3_f32 v92, v92, v55, v72
	s_waitcnt lgkmcnt(4)
	v_mfma_f32_32x32x16_bf16 v[20:35], v[88:91], v[164:167], v[20:35]
	v_max3_f32 v92, v92, v56, v73
	s_nop 0
	v_max3_f32 v92, v92, v57, v74
	s_nop 0
	v_max3_f32 v92, v92, v58, v75
	s_nop 0
	v_max3_f32 v92, v92, v59, v75
	s_waitcnt lgkmcnt(2)
	v_mfma_f32_32x32x16_bf16 v[4:19], v[84:87], v[100:103], v[4:19]
	s_waitcnt lgkmcnt(0)
	v_mfma_f32_32x32x16_bf16 v[20:35], v[84:87], v[104:107], v[20:35]
	v_max3_f32 v84, v92, v76, v60
	s_nop 0
	v_max3_f32 v84, v84, v77, v61
	s_nop 0
	v_max3_f32 v84, v84, v78, v62
	s_nop 0
	v_max3_f32 v84, v84, v79, v63
	s_nop 0
	v_max3_f32 v84, v84, v80, v64
	s_nop 0
	v_max3_f32 v84, v84, v81, v65
	s_nop 0
	v_max3_f32 v84, v84, v82, v66
	s_nop 0
	v_max3_f32 v84, v84, v83, v67
	s_nop 0
	v_mov_b32_e32 v85, v84
	s_nop 1
	v_permlane32_swap_b32_e32 v84, v85
	s_andn2_b64 vcc, exec, s[48:49]
	s_cbranch_vccnz .LBB0_1602
	v_max_f32_e32 v84, v84, v84
	v_max_f32_e32 v85, v85, v85
	v_max_f32_e32 v84, v84, v85
	v_cmp_lt_f32_e32 vcc, s13, v84
	s_cbranch_vccz .LBB0_1602
	v_max_f32_e32 v84, v84, v84
	v_max_f32_e32 v84, 0, v84
	v_exp_f32_e64 v85, -v84
	s_and_saveexec_b64 s[6:7], s[38:39]
	ds_write_b32 v2, v85
	s_or_b64 exec, exec, s[6:7]
	v_mul_f32_e32 v216, v216, v85
	s_waitcnt lgkmcnt(0)
	v_add_u32_e32 v85, s28, v190
	ds_read_b128 v[86:89], v85
	ds_read_b128 v[90:93], v85 offset:32
	ds_read_b128 v[94:97], v85 offset:64
	ds_read_b128 v[98:101], v85 offset:96
	s_waitcnt lgkmcnt(0)
	s_waitcnt lgkmcnt(3)
	v_pk_mul_f32 v[6:7], v[6:7], v[88:89]
	s_waitcnt lgkmcnt(2)
	v_pk_mul_f32 v[8:9], v[8:9], v[90:91]
	s_waitcnt lgkmcnt(1)
	v_pk_mul_f32 v[12:13], v[12:13], v[94:95]
	s_waitcnt lgkmcnt(0)
	v_pk_mul_f32 v[16:17], v[16:17], v[98:99]
	v_pk_mul_f32 v[18:19], v[18:19], v[100:101]
	v_pk_mul_f32 v[14:15], v[14:15], v[96:97]
	v_pk_mul_f32 v[10:11], v[10:11], v[92:93]
	v_pk_mul_f32 v[4:5], v[4:5], v[86:87]
	v_pk_mul_f32 v[32:33], v[32:33], v[98:99]
	v_pk_mul_f32 v[28:29], v[28:29], v[94:95]
	v_pk_mul_f32 v[24:25], v[24:25], v[90:91]
	v_pk_mul_f32 v[34:35], v[34:35], v[100:101]
	v_pk_mul_f32 v[30:31], v[30:31], v[96:97]
	v_pk_mul_f32 v[26:27], v[26:27], v[92:93]
	v_pk_mul_f32 v[22:23], v[22:23], v[88:89]
	v_pk_mul_f32 v[20:21], v[20:21], v[86:87]
	v_sub_f32_e32 v83, v83, v84
	v_sub_f32_e32 v82, v82, v84
	v_sub_f32_e32 v81, v81, v84
	v_sub_f32_e32 v80, v80, v84
	v_sub_f32_e32 v79, v79, v84
	v_sub_f32_e32 v78, v78, v84
	v_sub_f32_e32 v77, v77, v84
	v_sub_f32_e32 v76, v76, v84
	v_sub_f32_e32 v75, v75, v84
	v_sub_f32_e32 v74, v74, v84
	v_sub_f32_e32 v73, v73, v84
	v_sub_f32_e32 v72, v72, v84
	v_sub_f32_e32 v71, v71, v84
	v_sub_f32_e32 v70, v70, v84
	v_sub_f32_e32 v69, v69, v84
	v_sub_f32_e32 v68, v68, v84
	v_sub_f32_e32 v67, v67, v84
	v_sub_f32_e32 v66, v66, v84
	v_sub_f32_e32 v65, v65, v84
	v_sub_f32_e32 v64, v64, v84
	v_sub_f32_e32 v63, v63, v84
	v_sub_f32_e32 v62, v62, v84
	v_sub_f32_e32 v61, v61, v84
	v_sub_f32_e32 v60, v60, v84
	v_sub_f32_e32 v59, v59, v84
	v_sub_f32_e32 v58, v58, v84
	v_sub_f32_e32 v57, v57, v84
	v_sub_f32_e32 v56, v56, v84
	v_sub_f32_e32 v55, v55, v84
	v_sub_f32_e32 v54, v54, v84
	v_sub_f32_e32 v53, v53, v84
	v_sub_f32_e32 v52, v52, v84
	v_sub_f32_e32 v51, v51, v84
	v_sub_f32_e32 v50, v50, v84
	v_sub_f32_e32 v49, v49, v84
	v_sub_f32_e32 v48, v48, v84
	v_sub_f32_e32 v47, v47, v84
	v_sub_f32_e32 v46, v46, v84
	v_sub_f32_e32 v45, v45, v84
	v_sub_f32_e32 v44, v44, v84
	v_sub_f32_e32 v43, v43, v84
	v_sub_f32_e32 v42, v42, v84
	v_sub_f32_e32 v41, v41, v84
	v_sub_f32_e32 v40, v40, v84
	v_sub_f32_e32 v39, v39, v84
	v_sub_f32_e32 v38, v38, v84
	v_sub_f32_e32 v37, v37, v84
	v_sub_f32_e32 v36, v36, v84

.LBB0_1635:
	s_mul_i32 s2, s26, 0x3000
	v_add_u32_e32 v72, s2, v140
	ds_read_b128 v[68:71], v72 offset:12288
	ds_read_b128 v[148:151], v72 offset:12800
	ds_read_b128 v[152:155], v72 offset:14336
	ds_read_b128 v[156:159], v72 offset:14848
	ds_read_b128 v[160:163], v72 offset:16384
	ds_read_b128 v[164:167], v72 offset:16896
	ds_read_b128 v[168:171], v72 offset:18432
	ds_read_b128 v[172:175], v72 offset:18944
	s_waitcnt lgkmcnt(7)
	v_mfma_f32_32x32x16_bf16 v[100:115], v[68:71], v[116:119], v[36:51]
	v_exp_f32_e32 v84, v84
	v_exp_f32_e32 v85, v85
	v_exp_f32_e32 v86, v86
	v_exp_f32_e32 v87, v87
	v_exp_f32_e32 v88, v88
	v_exp_f32_e32 v89, v89
	v_pk_add_f32 v[144:145], v[84:85], 0 op_sel_hi:[1,0]
	s_waitcnt lgkmcnt(6)
	v_mfma_f32_32x32x16_bf16 v[68:83], v[148:151], v[116:119], v[36:51]
	v_add_f32_e64 v144, v86, v144
	v_add_f32_e64 v145, v87, v145
	v_add_f32_e64 v144, v88, v144
	v_add_f32_e64 v145, v89, v145
	s_waitcnt lgkmcnt(5)
	v_mfma_f32_32x32x16_bf16 v[100:115], v[152:155], v[120:123], v[100:115]
	v_exp_f32_e32 v90, v90
	v_exp_f32_e32 v91, v91
	v_exp_f32_e32 v92, v92
	v_exp_f32_e32 v93, v93
	v_exp_f32_e32 v94, v94
	v_exp_f32_e32 v95, v95
	v_pk_add_f32 v[144:145], v[90:91], v[144:145]
	s_waitcnt lgkmcnt(4)
	v_mfma_f32_32x32x16_bf16 v[68:83], v[156:159], v[120:123], v[68:83]
	v_add_f32_e64 v144, v92, v144
	v_add_f32_e64 v145, v93, v145
	v_add_f32_e64 v144, v94, v144
	v_add_f32_e64 v145, v95, v145
	s_waitcnt lgkmcnt(3)
	v_mfma_f32_32x32x16_bf16 v[100:115], v[160:163], v[124:127], v[100:115]
	v_exp_f32_e32 v96, v96
	v_exp_f32_e32 v97, v97
	v_exp_f32_e32 v98, v98
	v_exp_f32_e32 v99, v99
	v_exp_f32_e32 v148, v52
	v_exp_f32_e32 v149, v53
	v_pk_add_f32 v[144:145], v[96:97], v[144:145]
	s_waitcnt lgkmcnt(2)
	v_mfma_f32_32x32x16_bf16 v[68:83], v[164:167], v[124:127], v[68:83]
	v_add_f32_e64 v144, v98, v144
	v_add_f32_e64 v145, v99, v145
	v_add_f32_e64 v52, v148, v144
	v_add_f32_e64 v53, v149, v145
	s_waitcnt lgkmcnt(1)
	v_mfma_f32_32x32x16_bf16 v[100:115], v[168:171], v[128:131], v[100:115]
	v_exp_f32_e32 v144, v54
	v_exp_f32_e32 v145, v55
	v_exp_f32_e32 v150, v56
	v_exp_f32_e32 v151, v57
	v_exp_f32_e32 v152, v58
	v_exp_f32_e32 v153, v59
	v_pk_add_f32 v[52:53], v[144:145], v[52:53]
	s_waitcnt lgkmcnt(0)
	v_mfma_f32_32x32x16_bf16 v[68:83], v[172:175], v[128:131], v[68:83]
	v_add_f32_e64 v52, v150, v52
	v_add_f32_e64 v53, v151, v53
	v_add_f32_e64 v168, v152, v52
	v_add_f32_e64 v169, v153, v53
	v_cvt_pk_bf16_f32 v52, v84, v85
	v_cvt_pk_bf16_f32 v54, v88, v89
	v_cvt_pk_bf16_f32 v85, v144, v145
	v_lshl_add_u32 v144, s26, 13, v2
	ds_read_b64_tr_b16 v[88:89],v144 offset:0
	v_cvt_pk_bf16_f32 v55, v90, v91
	ds_read_b64_tr_b16 v[90:91],v144 offset:512
	v_cvt_pk_bf16_f32 v53, v86, v87
	v_cvt_pk_bf16_f32 v87, v152, v153
	ds_read_b64_tr_b16 v[152:153],v144 offset:4096
	ds_read_b64_tr_b16 v[154:155],v144 offset:4608
	v_cvt_pk_bf16_f32 v56, v92, v93
	ds_read_b64_tr_b16 v[92:93],v144 offset:1024
	v_cvt_pk_bf16_f32 v57, v94, v95
	ds_read_b64_tr_b16 v[94:95],v144 offset:1536
	ds_read_b64_tr_b16 v[156:157],v144 offset:5120
	ds_read_b64_tr_b16 v[158:159],v144 offset:5632
	v_cvt_pk_bf16_f32 v58, v96, v97
	ds_read_b64_tr_b16 v[96:97],v144 offset:2048
	v_cvt_pk_bf16_f32 v59, v98, v99
	ds_read_b64_tr_b16 v[98:99],v144 offset:2560
	ds_read_b64_tr_b16 v[160:161],v144 offset:6144
	ds_read_b64_tr_b16 v[162:163],v144 offset:6656
	v_cvt_pk_bf16_f32 v84, v148, v149
	ds_read_b64_tr_b16 v[148:149],v144 offset:3072
	v_cvt_pk_bf16_f32 v86, v150, v151
	ds_read_b64_tr_b16 v[150:151],v144 offset:3584
	ds_read_b64_tr_b16 v[164:165],v144 offset:7168
	ds_read_b64_tr_b16 v[166:167],v144 offset:7680
	s_waitcnt lgkmcnt(14)
	v_mfma_f32_32x32x16_bf16 v[4:19], v[52:55], v[88:91], v[4:19]
	s_waitcnt lgkmcnt(12)
	v_mfma_f32_32x32x16_bf16 v[20:35], v[52:55], v[152:155], v[20:35]
	v_exp_f32_e32 v52, v60
	v_exp_f32_e32 v53, v61
	v_exp_f32_e32 v60, v62
	v_exp_f32_e32 v61, v63
	v_pk_add_f32 v[54:55], v[52:53], v[168:169]
	s_nop 0
	v_pk_add_f32 v[54:55], v[60:61], v[54:55]
	s_waitcnt lgkmcnt(10)
	v_mfma_f32_32x32x16_bf16 v[4:19], v[56:59], v[92:95], v[4:19]
	v_cvt_pk_bf16_f32 v52, v52, v53
	v_cvt_pk_bf16_f32 v53, v60, v61
	s_waitcnt lgkmcnt(8)
	v_mfma_f32_32x32x16_bf16 v[20:35], v[56:59], v[156:159], v[20:35]
	v_exp_f32_e32 v56, v64
	v_exp_f32_e32 v57, v65
	v_exp_f32_e32 v58, v66
	v_exp_f32_e32 v59, v67
	v_pk_add_f32 v[54:55], v[56:57], v[54:55]
	s_nop 0
	v_pk_add_f32 v[62:63], v[58:59], v[54:55]
	v_cvt_pk_bf16_f32 v54, v56, v57
	v_add_f32_e32 v56, v62, v63
	v_add_f32_e32 v143, v143, v56
	v_cvt_pk_bf16_f32 v55, v58, v59
	s_waitcnt lgkmcnt(6)
	v_mfma_f32_32x32x16_bf16 v[4:19], v[84:87], v[96:99], v[4:19]
	v_max3_f32 v56, v100, v68, v101
	s_nop 0
	v_max3_f32 v56, v56, v69, v102
	s_nop 0
	v_max3_f32 v56, v56, v70, v103
	s_nop 0
	v_max3_f32 v56, v56, v71, v104
	s_waitcnt lgkmcnt(4)
	v_mfma_f32_32x32x16_bf16 v[20:35], v[84:87], v[160:163], v[20:35]
	v_max3_f32 v56, v56, v72, v105
	s_nop 0
	v_max3_f32 v56, v56, v73, v106
	s_nop 0
	v_max3_f32 v56, v56, v74, v107
	s_nop 0
	v_max3_f32 v56, v56, v75, v107
	s_waitcnt lgkmcnt(2)
	v_mfma_f32_32x32x16_bf16 v[4:19], v[52:55], v[148:151], v[4:19]
	s_waitcnt lgkmcnt(0)
	v_mfma_f32_32x32x16_bf16 v[20:35], v[52:55], v[164:167], v[20:35]
	v_max3_f32 v52, v56, v108, v76
	s_nop 0
	v_max3_f32 v52, v52, v109, v77
	s_nop 0
	v_max3_f32 v52, v52, v110, v78
	s_nop 0
	v_max3_f32 v52, v52, v111, v79
	s_nop 0
	v_max3_f32 v52, v52, v112, v80
	s_nop 0
	v_max3_f32 v52, v52, v113, v81
	s_nop 0
	v_max3_f32 v52, v52, v114, v82
	s_nop 0
	v_max3_f32 v52, v52, v115, v83
	s_nop 0
	v_mov_b32_e32 v53, v52
	s_nop 1
	v_permlane32_swap_b32_e32 v52, v53
	v_max_f32_e32 v53, v53, v53
	v_max_f32_e32 v52, v52, v52
	v_max_f32_e32 v52, v52, v53
	v_cmp_lt_f32_e32 vcc, s13, v52
	s_cbranch_vccz .LBB0_1639
	v_max_f32_e32 v52, v52, v52
	v_max_f32_e32 v52, 0, v52
	v_exp_f32_e64 v53, -v52
	s_and_saveexec_b64 s[6:7], s[36:37]
	ds_write_b32 v142, v53
	s_or_b64 exec, exec, s[6:7]
	v_mul_f32_e32 v143, v143, v53
	s_waitcnt lgkmcnt(0)
	v_add_u32_e32 v53, s24, v141
	ds_read_b128 v[54:57], v53
	ds_read_b128 v[58:61], v53 offset:32
	ds_read_b128 v[62:65], v53 offset:64
	ds_read_b128 v[84:87], v53 offset:96
	s_waitcnt lgkmcnt(0)
	s_waitcnt lgkmcnt(3)
	v_pk_mul_f32 v[6:7], v[6:7], v[56:57]
	s_waitcnt lgkmcnt(2)
	v_pk_mul_f32 v[8:9], v[8:9], v[58:59]
	s_waitcnt lgkmcnt(1)
	v_pk_mul_f32 v[12:13], v[12:13], v[62:63]
	s_waitcnt lgkmcnt(0)
	v_pk_mul_f32 v[16:17], v[16:17], v[84:85]
	v_pk_mul_f32 v[18:19], v[18:19], v[86:87]
	v_pk_mul_f32 v[14:15], v[14:15], v[64:65]
	v_pk_mul_f32 v[10:11], v[10:11], v[60:61]
	v_pk_mul_f32 v[4:5], v[4:5], v[54:55]
	v_pk_mul_f32 v[32:33], v[32:33], v[84:85]
	v_pk_mul_f32 v[28:29], v[28:29], v[62:63]
	v_pk_mul_f32 v[24:25], v[24:25], v[58:59]
	v_pk_mul_f32 v[34:35], v[34:35], v[86:87]
	v_pk_mul_f32 v[30:31], v[30:31], v[64:65]
	v_pk_mul_f32 v[26:27], v[26:27], v[60:61]
	v_pk_mul_f32 v[22:23], v[22:23], v[56:57]
	v_pk_mul_f32 v[20:21], v[20:21], v[54:55]
	v_sub_f32_e32 v115, v115, v52
	v_sub_f32_e32 v114, v114, v52
	v_sub_f32_e32 v113, v113, v52
	v_sub_f32_e32 v112, v112, v52
	v_sub_f32_e32 v111, v111, v52
	v_sub_f32_e32 v110, v110, v52
	v_sub_f32_e32 v109, v109, v52
	v_sub_f32_e32 v108, v108, v52
	v_sub_f32_e32 v107, v107, v52
	v_sub_f32_e32 v106, v106, v52
	v_sub_f32_e32 v105, v105, v52
	v_sub_f32_e32 v104, v104, v52
	v_sub_f32_e32 v103, v103, v52
	v_sub_f32_e32 v102, v102, v52
	v_sub_f32_e32 v101, v101, v52
	v_sub_f32_e32 v100, v100, v52
	v_sub_f32_e32 v83, v83, v52
	v_sub_f32_e32 v82, v82, v52
	v_sub_f32_e32 v81, v81, v52
	v_sub_f32_e32 v80, v80, v52
	v_sub_f32_e32 v79, v79, v52
	v_sub_f32_e32 v78, v78, v52
	v_sub_f32_e32 v77, v77, v52
	v_sub_f32_e32 v76, v76, v52
	v_sub_f32_e32 v75, v75, v52
	v_sub_f32_e32 v74, v74, v52
	v_sub_f32_e32 v73, v73, v52
	v_sub_f32_e32 v72, v72, v52
	v_sub_f32_e32 v71, v71, v52
	v_sub_f32_e32 v70, v70, v52
	v_sub_f32_e32 v69, v69, v52
	v_sub_f32_e32 v68, v68, v52
	v_sub_f32_e32 v51, v51, v52
	v_sub_f32_e32 v50, v50, v52
	v_sub_f32_e32 v49, v49, v52
	v_sub_f32_e32 v48, v48, v52
	v_sub_f32_e32 v47, v47, v52
	v_sub_f32_e32 v46, v46, v52
	v_sub_f32_e32 v45, v45, v52
	v_sub_f32_e32 v44, v44, v52
	v_sub_f32_e32 v43, v43, v52
	v_sub_f32_e32 v42, v42, v52
	v_sub_f32_e32 v41, v41, v52
	v_sub_f32_e32 v40, v40, v52
	v_sub_f32_e32 v39, v39, v52
	v_sub_f32_e32 v38, v38, v52
	v_sub_f32_e32 v37, v37, v52
	v_sub_f32_e32 v36, v36, v52

.LBB0_1643:
	s_xor_b32 s2, s26, 2
	s_mulk_i32 s2, 0x3000
	v_add_u32_e32 v56, s2, v140
	ds_read_b128 v[52:55], v56
	ds_read_b128 v[148:151], v56 offset:512
	ds_read_b128 v[152:155], v56 offset:2048
	ds_read_b128 v[156:159], v56 offset:2560
	ds_read_b128 v[160:163], v56 offset:4096
	ds_read_b128 v[164:167], v56 offset:4608
	ds_read_b128 v[168:171], v56 offset:6144
	ds_read_b128 v[172:175], v56 offset:6656
	s_waitcnt lgkmcnt(7)
	v_mfma_f32_32x32x16_bf16 v[84:99], v[52:55], v[116:119], v[36:51]
	v_exp_f32_e32 v100, v100
	v_exp_f32_e32 v101, v101
	v_exp_f32_e32 v102, v102
	v_exp_f32_e32 v103, v103
	v_exp_f32_e32 v104, v104
	v_exp_f32_e32 v105, v105
	s_waitcnt lgkmcnt(6)
	v_mfma_f32_32x32x16_bf16 v[52:67], v[148:151], v[116:119], v[36:51]
	v_add_f32_e64 v148, v100, 0
	v_add_f32_e64 v149, v101, 0
	v_add_f32_e64 v148, v102, v148
	v_add_f32_e64 v149, v103, v149
	v_add_f32_e64 v148, v104, v148
	v_add_f32_e64 v149, v105, v149
	s_waitcnt lgkmcnt(5)
	v_mfma_f32_32x32x16_bf16 v[84:99], v[152:155], v[120:123], v[84:99]
	v_exp_f32_e32 v106, v106
	v_exp_f32_e32 v107, v107
	v_exp_f32_e32 v108, v108
	v_exp_f32_e32 v109, v109
	v_exp_f32_e32 v110, v110
	v_exp_f32_e32 v111, v111
	v_pk_add_f32 v[148:149], v[106:107], v[148:149]
	s_waitcnt lgkmcnt(4)
	v_mfma_f32_32x32x16_bf16 v[52:67], v[156:159], v[120:123], v[52:67]
	v_add_f32_e64 v148, v108, v148
	v_add_f32_e64 v149, v109, v149
	v_add_f32_e64 v148, v110, v148
	v_add_f32_e64 v149, v111, v149
	s_waitcnt lgkmcnt(3)
	v_mfma_f32_32x32x16_bf16 v[84:99], v[160:163], v[124:127], v[84:99]
	v_exp_f32_e32 v112, v112
	v_exp_f32_e32 v113, v113
	v_exp_f32_e32 v114, v114
	v_exp_f32_e32 v115, v115
	v_exp_f32_e32 v150, v68
	v_exp_f32_e32 v151, v69
	v_pk_add_f32 v[148:149], v[112:113], v[148:149]
	s_waitcnt lgkmcnt(2)
	v_mfma_f32_32x32x16_bf16 v[52:67], v[164:167], v[124:127], v[52:67]
	v_add_f32_e64 v148, v114, v148
	v_add_f32_e64 v149, v115, v149
	v_add_f32_e64 v68, v150, v148
	v_add_f32_e64 v69, v151, v149
	s_waitcnt lgkmcnt(1)
	v_mfma_f32_32x32x16_bf16 v[84:99], v[168:171], v[128:131], v[84:99]
	v_exp_f32_e32 v148, v70
	v_exp_f32_e32 v149, v71
	v_exp_f32_e32 v152, v72
	v_exp_f32_e32 v153, v73
	v_exp_f32_e32 v154, v74
	v_exp_f32_e32 v155, v75
	v_pk_add_f32 v[68:69], v[148:149], v[68:69]
	s_waitcnt lgkmcnt(0)
	v_mfma_f32_32x32x16_bf16 v[52:67], v[172:175], v[128:131], v[52:67]
	v_add_f32_e64 v68, v152, v68
	v_add_f32_e64 v69, v153, v69
	v_add_f32_e64 v168, v154, v68
	v_add_f32_e64 v169, v155, v69
	v_add_u32_e32 v144, 0x2000, v144
	v_cvt_pk_bf16_f32 v70, v104, v105
	ds_read_b64_tr_b16 v[104:105],v144 offset:0
	v_cvt_pk_bf16_f32 v71, v106, v107
	ds_read_b64_tr_b16 v[106:107],v144 offset:512
	v_cvt_pk_bf16_f32 v69, v102, v103
	v_cvt_pk_bf16_f32 v102, v152, v153
	ds_read_b64_tr_b16 v[152:153],v144 offset:4096
	v_cvt_pk_bf16_f32 v103, v154, v155
	ds_read_b64_tr_b16 v[154:155],v144 offset:4608
	v_cvt_pk_bf16_f32 v72, v108, v109
	ds_read_b64_tr_b16 v[108:109],v144 offset:1024
	v_cvt_pk_bf16_f32 v73, v110, v111
	ds_read_b64_tr_b16 v[110:111],v144 offset:1536
	ds_read_b64_tr_b16 v[156:157],v144 offset:5120
	ds_read_b64_tr_b16 v[158:159],v144 offset:5632
	v_cvt_pk_bf16_f32 v74, v112, v113
	ds_read_b64_tr_b16 v[112:113],v144 offset:2048
	v_cvt_pk_bf16_f32 v75, v114, v115
	ds_read_b64_tr_b16 v[114:115],v144 offset:2560
	ds_read_b64_tr_b16 v[160:161],v144 offset:6144
	ds_read_b64_tr_b16 v[162:163],v144 offset:6656
	v_cvt_pk_bf16_f32 v68, v100, v101
	v_cvt_pk_bf16_f32 v101, v148, v149
	ds_read_b64_tr_b16 v[148:149],v144 offset:3072
	v_cvt_pk_bf16_f32 v100, v150, v151
	ds_read_b64_tr_b16 v[150:151],v144 offset:3584
	ds_read_b64_tr_b16 v[164:165],v144 offset:7168
	ds_read_b64_tr_b16 v[166:167],v144 offset:7680
	s_waitcnt lgkmcnt(14)
	v_mfma_f32_32x32x16_bf16 v[4:19], v[68:71], v[104:107], v[4:19]
	s_waitcnt lgkmcnt(12)
	v_mfma_f32_32x32x16_bf16 v[20:35], v[68:71], v[152:155], v[20:35]
	v_exp_f32_e32 v68, v76
	v_exp_f32_e32 v69, v77
	v_exp_f32_e32 v76, v78
	v_exp_f32_e32 v77, v79
	v_pk_add_f32 v[70:71], v[68:69], v[168:169]
	s_nop 0
	v_pk_add_f32 v[70:71], v[76:77], v[70:71]
	s_waitcnt lgkmcnt(10)
	v_mfma_f32_32x32x16_bf16 v[4:19], v[72:75], v[108:111], v[4:19]
	v_cvt_pk_bf16_f32 v68, v68, v69
	v_cvt_pk_bf16_f32 v69, v76, v77
	s_waitcnt lgkmcnt(8)
	v_mfma_f32_32x32x16_bf16 v[20:35], v[72:75], v[156:159], v[20:35]
	v_exp_f32_e32 v72, v80
	v_exp_f32_e32 v73, v81
	v_exp_f32_e32 v74, v82
	v_exp_f32_e32 v75, v83
	v_pk_add_f32 v[70:71], v[72:73], v[70:71]
	s_nop 0
	v_pk_add_f32 v[78:79], v[74:75], v[70:71]
	v_cvt_pk_bf16_f32 v70, v72, v73
	v_add_f32_e32 v72, v78, v79
	v_add_f32_e32 v143, v143, v72
	v_cvt_pk_bf16_f32 v71, v74, v75
	s_waitcnt lgkmcnt(6)
	v_mfma_f32_32x32x16_bf16 v[4:19], v[100:103], v[112:115], v[4:19]
	v_max3_f32 v72, v84, v52, v85
	s_nop 0
	v_max3_f32 v72, v72, v53, v86
	s_nop 0
	v_max3_f32 v72, v72, v54, v87
	s_nop 0
	v_max3_f32 v72, v72, v55, v88
	s_waitcnt lgkmcnt(4)
	v_mfma_f32_32x32x16_bf16 v[20:35], v[100:103], v[160:163], v[20:35]
	v_max3_f32 v72, v72, v56, v89
	s_nop 0
	v_max3_f32 v72, v72, v57, v90
	s_nop 0
	v_max3_f32 v72, v72, v58, v91
	s_nop 0
	v_max3_f32 v72, v72, v59, v91
	s_waitcnt lgkmcnt(2)
	v_mfma_f32_32x32x16_bf16 v[4:19], v[68:71], v[148:151], v[4:19]
	s_waitcnt lgkmcnt(0)
	v_mfma_f32_32x32x16_bf16 v[20:35], v[68:71], v[164:167], v[20:35]
	v_max3_f32 v68, v72, v92, v60
	s_nop 0
	v_max3_f32 v68, v68, v93, v61
	s_nop 0
	v_max3_f32 v68, v68, v94, v62
	s_nop 0
	v_max3_f32 v68, v68, v95, v63
	s_nop 0
	v_max3_f32 v68, v68, v96, v64
	s_nop 0
	v_max3_f32 v68, v68, v97, v65
	s_nop 0
	v_max3_f32 v68, v68, v98, v66
	s_nop 0
	v_max3_f32 v68, v68, v99, v67
	s_nop 0
	v_mov_b32_e32 v69, v68
	s_nop 1
	v_permlane32_swap_b32_e32 v68, v69
	s_and_b64 vcc, exec, s[38:39]
	s_cbranch_vccnz .LBB0_1630
	v_max_f32_e32 v68, v68, v68
	v_max_f32_e32 v69, v69, v69
	v_max_f32_e32 v68, v68, v69
	v_cmp_lt_f32_e32 vcc, s13, v68
	s_cbranch_vccz .LBB0_1630
	v_max_f32_e32 v68, v68, v68
	v_max_f32_e32 v68, 0, v68
	v_exp_f32_e64 v69, -v68
	s_and_saveexec_b64 s[6:7], s[36:37]
	s_cbranch_execz .LBB0_1629
	ds_write_b32 v142, v69
	s_branch .LBB0_1629

.LBB0_1667:
	s_or_b32 s25, s26, 1
	s_mul_i32 s2, s25, 0x3000
	v_add_u32_e32 v72, s2, v151
	ds_read_b128 v[68:71], v72
	ds_read_b128 v[156:159], v72 offset:512
	ds_read_b128 v[160:163], v72 offset:2048
	ds_read_b128 v[164:167], v72 offset:2560
	ds_read_b128 v[168:171], v72 offset:4096
	ds_read_b128 v[172:175], v72 offset:4608
	ds_read_b128 v[176:179], v72 offset:6144
	ds_read_b128 v[180:183], v72 offset:6656
	ds_read_b128 v[184:187], v72 offset:8192
	ds_read_b128 v[190:193], v72 offset:8704
	ds_read_b128 v[212:215], v72 offset:10240
	ds_read_b128 v[216:219], v72 offset:10752
	s_waitcnt lgkmcnt(11)
	v_mfma_f32_32x32x16_bf16 v[100:115], v[68:71], v[116:119], v[36:51]
	v_exp_f32_e32 v84, v84
	v_exp_f32_e32 v85, v85
	v_exp_f32_e32 v86, v86
	v_exp_f32_e32 v87, v87
	s_waitcnt lgkmcnt(10)
	v_mfma_f32_32x32x16_bf16 v[68:83], v[156:159], v[116:119], v[36:51]
	v_add_f32_e64 v156, v84, 0
	v_add_f32_e64 v157, v85, 0
	v_add_f32_e64 v156, v86, v156
	v_add_f32_e64 v157, v87, v157
	s_waitcnt lgkmcnt(9)
	v_mfma_f32_32x32x16_bf16 v[100:115], v[160:163], v[120:123], v[100:115]
	v_exp_f32_e32 v88, v88
	v_exp_f32_e32 v89, v89
	v_exp_f32_e32 v90, v90
	v_exp_f32_e32 v91, v91
	v_pk_add_f32 v[156:157], v[88:89], v[156:157]
	s_nop 0
	v_pk_add_f32 v[156:157], v[90:91], v[156:157]
	s_waitcnt lgkmcnt(8)
	v_mfma_f32_32x32x16_bf16 v[68:83], v[164:167], v[120:123], v[68:83]
	s_waitcnt lgkmcnt(7)
	v_mfma_f32_32x32x16_bf16 v[100:115], v[168:171], v[124:127], v[100:115]
	v_exp_f32_e32 v92, v92
	v_exp_f32_e32 v93, v93
	v_exp_f32_e32 v94, v94
	v_exp_f32_e32 v95, v95
	v_pk_add_f32 v[156:157], v[92:93], v[156:157]
	s_nop 0
	v_pk_add_f32 v[156:157], v[94:95], v[156:157]
	s_waitcnt lgkmcnt(6)
	v_mfma_f32_32x32x16_bf16 v[68:83], v[172:175], v[124:127], v[68:83]
	s_waitcnt lgkmcnt(5)
	v_mfma_f32_32x32x16_bf16 v[100:115], v[176:179], v[128:131], v[100:115]
	v_exp_f32_e32 v96, v96
	v_exp_f32_e32 v97, v97
	v_exp_f32_e32 v98, v98
	v_exp_f32_e32 v99, v99
	v_pk_add_f32 v[156:157], v[96:97], v[156:157]
	s_nop 0
	v_pk_add_f32 v[156:157], v[98:99], v[156:157]
	s_waitcnt lgkmcnt(4)
	v_mfma_f32_32x32x16_bf16 v[68:83], v[180:183], v[128:131], v[68:83]
	v_exp_f32_e32 v158, v52
	v_exp_f32_e32 v159, v53
	s_waitcnt lgkmcnt(3)
	v_mfma_f32_32x32x16_bf16 v[100:115], v[184:187], v[132:135], v[100:115]
	v_add_f32_e64 v52, v158, v156
	v_add_f32_e64 v53, v159, v157
	v_exp_f32_e32 v156, v54
	v_exp_f32_e32 v157, v55
	s_nop 0
	v_pk_add_f32 v[52:53], v[156:157], v[52:53]
	s_waitcnt lgkmcnt(2)
	v_mfma_f32_32x32x16_bf16 v[68:83], v[190:193], v[132:135], v[68:83]
	s_waitcnt lgkmcnt(1)
	v_mfma_f32_32x32x16_bf16 v[100:115], v[212:215], v[136:139], v[100:115]
	v_exp_f32_e32 v160, v56
	v_exp_f32_e32 v161, v57
	v_exp_f32_e32 v162, v58
	v_exp_f32_e32 v163, v59
	v_pk_add_f32 v[52:53], v[160:161], v[52:53]
	s_nop 0
	v_pk_add_f32 v[176:177], v[162:163], v[52:53]
	s_waitcnt lgkmcnt(0)
	v_mfma_f32_32x32x16_bf16 v[68:83], v[216:219], v[136:139], v[68:83]
	v_cvt_pk_bf16_f32 v54, v88, v89
	v_lshl_add_u32 v155, s26, 13, v2
	ds_read_b64_tr_b16 v[88:89],v155 offset:0
	v_cvt_pk_bf16_f32 v55, v90, v91
	ds_read_b64_tr_b16 v[90:91],v155 offset:512
	v_cvt_pk_bf16_f32 v53, v86, v87
	v_cvt_pk_bf16_f32 v86, v160, v161
	ds_read_b64_tr_b16 v[160:161],v155 offset:4096
	v_cvt_pk_bf16_f32 v87, v162, v163
	ds_read_b64_tr_b16 v[162:163],v155 offset:4608
	v_cvt_pk_bf16_f32 v56, v92, v93
	ds_read_b64_tr_b16 v[92:93],v155 offset:1024
	v_cvt_pk_bf16_f32 v57, v94, v95
	ds_read_b64_tr_b16 v[94:95],v155 offset:1536
	ds_read_b64_tr_b16 v[164:165],v155 offset:5120
	ds_read_b64_tr_b16 v[166:167],v155 offset:5632
	v_cvt_pk_bf16_f32 v58, v96, v97
	ds_read_b64_tr_b16 v[96:97],v155 offset:2048
	v_cvt_pk_bf16_f32 v59, v98, v99
	ds_read_b64_tr_b16 v[98:99],v155 offset:2560
	ds_read_b64_tr_b16 v[168:169],v155 offset:6144
	ds_read_b64_tr_b16 v[170:171],v155 offset:6656
	v_cvt_pk_bf16_f32 v52, v84, v85
	v_cvt_pk_bf16_f32 v85, v156, v157
	ds_read_b64_tr_b16 v[156:157],v155 offset:3072
	v_cvt_pk_bf16_f32 v84, v158, v159
	ds_read_b64_tr_b16 v[158:159],v155 offset:3584
	ds_read_b64_tr_b16 v[172:173],v155 offset:7168
	ds_read_b64_tr_b16 v[174:175],v155 offset:7680
	s_waitcnt lgkmcnt(14)
	v_mfma_f32_32x32x16_bf16 v[4:19], v[52:55], v[88:91], v[4:19]
	s_waitcnt lgkmcnt(12)
	v_mfma_f32_32x32x16_bf16 v[20:35], v[52:55], v[160:163], v[20:35]
	v_exp_f32_e32 v52, v60
	v_exp_f32_e32 v53, v61
	v_exp_f32_e32 v60, v62
	v_exp_f32_e32 v61, v63
	v_pk_add_f32 v[54:55], v[52:53], v[176:177]
	s_nop 0
	v_pk_add_f32 v[54:55], v[60:61], v[54:55]
	s_waitcnt lgkmcnt(10)
	v_mfma_f32_32x32x16_bf16 v[4:19], v[56:59], v[92:95], v[4:19]
	v_cvt_pk_bf16_f32 v52, v52, v53
	v_cvt_pk_bf16_f32 v53, v60, v61
	s_waitcnt lgkmcnt(8)
	v_mfma_f32_32x32x16_bf16 v[20:35], v[56:59], v[164:167], v[20:35]
	v_exp_f32_e32 v56, v64
	v_exp_f32_e32 v57, v65
	v_exp_f32_e32 v58, v66
	v_exp_f32_e32 v59, v67
	v_pk_add_f32 v[54:55], v[56:57], v[54:55]
	s_nop 0
	v_pk_add_f32 v[62:63], v[58:59], v[54:55]
	v_cvt_pk_bf16_f32 v54, v56, v57
	v_add_f32_e32 v56, v62, v63
	v_add_f32_e32 v154, v154, v56
	v_cvt_pk_bf16_f32 v55, v58, v59
	s_waitcnt lgkmcnt(6)
	v_mfma_f32_32x32x16_bf16 v[4:19], v[84:87], v[96:99], v[4:19]
	v_max3_f32 v56, v100, v68, v101
	s_nop 0
	v_max3_f32 v56, v56, v69, v102
	s_nop 0
	v_max3_f32 v56, v56, v70, v103
	s_nop 0
	v_max3_f32 v56, v56, v71, v104
	s_waitcnt lgkmcnt(4)
	v_mfma_f32_32x32x16_bf16 v[20:35], v[84:87], v[168:171], v[20:35]
	v_max3_f32 v56, v56, v72, v105
	s_nop 0
	v_max3_f32 v56, v56, v73, v106
	s_nop 0
	v_max3_f32 v56, v56, v74, v107
	s_nop 0
	v_max3_f32 v56, v56, v75, v107
	s_waitcnt lgkmcnt(2)
	v_mfma_f32_32x32x16_bf16 v[4:19], v[52:55], v[156:159], v[4:19]
	s_waitcnt lgkmcnt(0)
	v_mfma_f32_32x32x16_bf16 v[20:35], v[52:55], v[172:175], v[20:35]
	v_max3_f32 v52, v56, v108, v76
	s_nop 0
	v_max3_f32 v52, v52, v109, v77
	s_nop 0
	v_max3_f32 v52, v52, v110, v78
	s_nop 0
	v_max3_f32 v52, v52, v111, v79
	s_nop 0
	v_max3_f32 v52, v52, v112, v80
	s_nop 0
	v_max3_f32 v52, v52, v113, v81
	s_nop 0
	v_max3_f32 v52, v52, v114, v82
	s_nop 0
	v_max3_f32 v52, v52, v115, v83
	s_nop 0
	v_mov_b32_e32 v53, v52
	s_nop 1
	v_permlane32_swap_b32_e32 v52, v53
	v_max_f32_e32 v53, v53, v53
	v_max_f32_e32 v52, v52, v52
	v_max_f32_e32 v52, v52, v53
	v_cmp_lt_f32_e32 vcc, s13, v52
	s_cbranch_vccz .LBB0_1671
	v_max_f32_e32 v52, v52, v52
	v_max_f32_e32 v52, 0, v52
	v_exp_f32_e64 v53, -v52
	s_and_saveexec_b64 s[6:7], s[36:37]
	ds_write_b32 v153, v53
	s_or_b64 exec, exec, s[6:7]
	v_mul_f32_e32 v154, v154, v53
	s_waitcnt lgkmcnt(0)
	v_add_u32_e32 v53, s24, v152
	ds_read_b128 v[54:57], v53
	ds_read_b128 v[58:61], v53 offset:32
	ds_read_b128 v[62:65], v53 offset:64
	ds_read_b128 v[84:87], v53 offset:96
	s_waitcnt lgkmcnt(0)
	s_waitcnt lgkmcnt(3)
	v_pk_mul_f32 v[6:7], v[6:7], v[56:57]
	s_waitcnt lgkmcnt(2)
	v_pk_mul_f32 v[8:9], v[8:9], v[58:59]
	s_waitcnt lgkmcnt(1)
	v_pk_mul_f32 v[12:13], v[12:13], v[62:63]
	s_waitcnt lgkmcnt(0)
	v_pk_mul_f32 v[16:17], v[16:17], v[84:85]
	v_pk_mul_f32 v[18:19], v[18:19], v[86:87]
	v_pk_mul_f32 v[14:15], v[14:15], v[64:65]
	v_pk_mul_f32 v[10:11], v[10:11], v[60:61]
	v_pk_mul_f32 v[4:5], v[4:5], v[54:55]
	v_pk_mul_f32 v[32:33], v[32:33], v[84:85]
	v_pk_mul_f32 v[28:29], v[28:29], v[62:63]
	v_pk_mul_f32 v[24:25], v[24:25], v[58:59]
	v_pk_mul_f32 v[34:35], v[34:35], v[86:87]
	v_pk_mul_f32 v[30:31], v[30:31], v[64:65]
	v_pk_mul_f32 v[26:27], v[26:27], v[60:61]
	v_pk_mul_f32 v[22:23], v[22:23], v[56:57]
	v_pk_mul_f32 v[20:21], v[20:21], v[54:55]
	v_sub_f32_e32 v115, v115, v52
	v_sub_f32_e32 v114, v114, v52
	v_sub_f32_e32 v113, v113, v52
	v_sub_f32_e32 v112, v112, v52
	v_sub_f32_e32 v111, v111, v52
	v_sub_f32_e32 v110, v110, v52
	v_sub_f32_e32 v109, v109, v52
	v_sub_f32_e32 v108, v108, v52
	v_sub_f32_e32 v107, v107, v52
	v_sub_f32_e32 v106, v106, v52
	v_sub_f32_e32 v105, v105, v52
	v_sub_f32_e32 v104, v104, v52
	v_sub_f32_e32 v103, v103, v52
	v_sub_f32_e32 v102, v102, v52
	v_sub_f32_e32 v101, v101, v52
	v_sub_f32_e32 v100, v100, v52
	v_sub_f32_e32 v83, v83, v52
	v_sub_f32_e32 v82, v82, v52
	v_sub_f32_e32 v81, v81, v52
	v_sub_f32_e32 v80, v80, v52
	v_sub_f32_e32 v79, v79, v52
	v_sub_f32_e32 v78, v78, v52
	v_sub_f32_e32 v77, v77, v52
	v_sub_f32_e32 v76, v76, v52
	v_sub_f32_e32 v75, v75, v52
	v_sub_f32_e32 v74, v74, v52
	v_sub_f32_e32 v73, v73, v52
	v_sub_f32_e32 v72, v72, v52
	v_sub_f32_e32 v71, v71, v52
	v_sub_f32_e32 v70, v70, v52
	v_sub_f32_e32 v69, v69, v52
	v_sub_f32_e32 v68, v68, v52
	v_sub_f32_e32 v51, v51, v52
	v_sub_f32_e32 v50, v50, v52
	v_sub_f32_e32 v49, v49, v52
	v_sub_f32_e32 v48, v48, v52
	v_sub_f32_e32 v47, v47, v52
	v_sub_f32_e32 v46, v46, v52
	v_sub_f32_e32 v45, v45, v52
	v_sub_f32_e32 v44, v44, v52
	v_sub_f32_e32 v43, v43, v52
	v_sub_f32_e32 v42, v42, v52
	v_sub_f32_e32 v41, v41, v52
	v_sub_f32_e32 v40, v40, v52
	v_sub_f32_e32 v39, v39, v52
	v_sub_f32_e32 v38, v38, v52
	v_sub_f32_e32 v37, v37, v52
	v_sub_f32_e32 v36, v36, v52

.LBB0_1675:
	s_xor_b32 s2, s26, 2
	s_mulk_i32 s2, 0x3000
	v_add_u32_e32 v56, s2, v151
	ds_read_b128 v[52:55], v56
	ds_read_b128 v[156:159], v56 offset:512
	ds_read_b128 v[160:163], v56 offset:2048
	ds_read_b128 v[164:167], v56 offset:2560
	ds_read_b128 v[168:171], v56 offset:4096
	ds_read_b128 v[172:175], v56 offset:4608
	ds_read_b128 v[176:179], v56 offset:6144
	ds_read_b128 v[180:183], v56 offset:6656
	ds_read_b128 v[184:187], v56 offset:8192
	ds_read_b128 v[190:193], v56 offset:8704
	ds_read_b128 v[212:215], v56 offset:10240
	ds_read_b128 v[216:219], v56 offset:10752
	s_waitcnt lgkmcnt(11)
	v_mfma_f32_32x32x16_bf16 v[84:99], v[52:55], v[116:119], v[36:51]
	v_exp_f32_e32 v100, v100
	v_exp_f32_e32 v101, v101
	v_exp_f32_e32 v102, v102
	v_exp_f32_e32 v103, v103
	s_waitcnt lgkmcnt(10)
	v_mfma_f32_32x32x16_bf16 v[52:67], v[156:159], v[116:119], v[36:51]
	v_add_f32_e64 v156, v100, 0
	v_add_f32_e64 v157, v101, 0
	v_add_f32_e64 v156, v102, v156
	v_add_f32_e64 v157, v103, v157
	s_waitcnt lgkmcnt(9)
	v_mfma_f32_32x32x16_bf16 v[84:99], v[160:163], v[120:123], v[84:99]
	v_exp_f32_e32 v104, v104
	v_exp_f32_e32 v105, v105
	v_exp_f32_e32 v106, v106
	v_exp_f32_e32 v107, v107
	v_pk_add_f32 v[156:157], v[104:105], v[156:157]
	s_nop 0
	v_pk_add_f32 v[156:157], v[106:107], v[156:157]
	s_waitcnt lgkmcnt(8)
	v_mfma_f32_32x32x16_bf16 v[52:67], v[164:167], v[120:123], v[52:67]
	s_waitcnt lgkmcnt(7)
	v_mfma_f32_32x32x16_bf16 v[84:99], v[168:171], v[124:127], v[84:99]
	v_exp_f32_e32 v108, v108
	v_exp_f32_e32 v109, v109
	v_exp_f32_e32 v110, v110
	v_exp_f32_e32 v111, v111
	v_pk_add_f32 v[156:157], v[108:109], v[156:157]
	s_nop 0
	v_pk_add_f32 v[156:157], v[110:111], v[156:157]
	s_waitcnt lgkmcnt(6)
	v_mfma_f32_32x32x16_bf16 v[52:67], v[172:175], v[124:127], v[52:67]
	s_waitcnt lgkmcnt(5)
	v_mfma_f32_32x32x16_bf16 v[84:99], v[176:179], v[128:131], v[84:99]
	v_exp_f32_e32 v112, v112
	v_exp_f32_e32 v113, v113
	v_exp_f32_e32 v114, v114
	v_exp_f32_e32 v115, v115
	v_pk_add_f32 v[156:157], v[112:113], v[156:157]
	s_nop 0
	v_pk_add_f32 v[156:157], v[114:115], v[156:157]
	s_waitcnt lgkmcnt(4)
	v_mfma_f32_32x32x16_bf16 v[52:67], v[180:183], v[128:131], v[52:67]
	v_exp_f32_e32 v158, v68
	v_exp_f32_e32 v159, v69
	s_waitcnt lgkmcnt(3)
	v_mfma_f32_32x32x16_bf16 v[84:99], v[184:187], v[132:135], v[84:99]
	v_add_f32_e64 v68, v158, v156
	v_add_f32_e64 v69, v159, v157
	v_exp_f32_e32 v156, v70
	v_exp_f32_e32 v157, v71
	s_nop 0
	v_pk_add_f32 v[68:69], v[156:157], v[68:69]
	s_waitcnt lgkmcnt(2)
	v_mfma_f32_32x32x16_bf16 v[52:67], v[190:193], v[132:135], v[52:67]
	s_waitcnt lgkmcnt(1)
	v_mfma_f32_32x32x16_bf16 v[84:99], v[212:215], v[136:139], v[84:99]
	v_exp_f32_e32 v160, v72
	v_exp_f32_e32 v161, v73
	v_exp_f32_e32 v162, v74
	v_exp_f32_e32 v163, v75
	v_pk_add_f32 v[68:69], v[160:161], v[68:69]
	s_nop 0
	v_pk_add_f32 v[176:177], v[162:163], v[68:69]
	s_waitcnt lgkmcnt(0)
	v_mfma_f32_32x32x16_bf16 v[52:67], v[216:219], v[136:139], v[52:67]
	v_cvt_pk_bf16_f32 v70, v104, v105
	v_lshl_add_u32 v155, s25, 13, v2
	ds_read_b64_tr_b16 v[104:105],v155 offset:0
	v_cvt_pk_bf16_f32 v71, v106, v107
	ds_read_b64_tr_b16 v[106:107],v155 offset:512
	v_cvt_pk_bf16_f32 v69, v102, v103
	v_cvt_pk_bf16_f32 v102, v160, v161
	ds_read_b64_tr_b16 v[160:161],v155 offset:4096
	v_cvt_pk_bf16_f32 v103, v162, v163
	ds_read_b64_tr_b16 v[162:163],v155 offset:4608
	v_cvt_pk_bf16_f32 v72, v108, v109
	ds_read_b64_tr_b16 v[108:109],v155 offset:1024
	v_cvt_pk_bf16_f32 v73, v110, v111
	ds_read_b64_tr_b16 v[110:111],v155 offset:1536
	ds_read_b64_tr_b16 v[164:165],v155 offset:5120
	ds_read_b64_tr_b16 v[166:167],v155 offset:5632
	v_cvt_pk_bf16_f32 v74, v112, v113
	ds_read_b64_tr_b16 v[112:113],v155 offset:2048
	v_cvt_pk_bf16_f32 v75, v114, v115
	ds_read_b64_tr_b16 v[114:115],v155 offset:2560
	ds_read_b64_tr_b16 v[168:169],v155 offset:6144
	ds_read_b64_tr_b16 v[170:171],v155 offset:6656
	v_cvt_pk_bf16_f32 v68, v100, v101
	v_cvt_pk_bf16_f32 v101, v156, v157
	ds_read_b64_tr_b16 v[156:157],v155 offset:3072
	v_cvt_pk_bf16_f32 v100, v158, v159
	ds_read_b64_tr_b16 v[158:159],v155 offset:3584
	ds_read_b64_tr_b16 v[172:173],v155 offset:7168
	ds_read_b64_tr_b16 v[174:175],v155 offset:7680
	s_waitcnt lgkmcnt(14)
	v_mfma_f32_32x32x16_bf16 v[4:19], v[68:71], v[104:107], v[4:19]
	s_waitcnt lgkmcnt(12)
	v_mfma_f32_32x32x16_bf16 v[20:35], v[68:71], v[160:163], v[20:35]
	v_exp_f32_e32 v68, v76
	v_exp_f32_e32 v69, v77
	v_exp_f32_e32 v76, v78
	v_exp_f32_e32 v77, v79
	v_pk_add_f32 v[70:71], v[68:69], v[176:177]
	s_nop 0
	v_pk_add_f32 v[70:71], v[76:77], v[70:71]
	s_waitcnt lgkmcnt(10)
	v_mfma_f32_32x32x16_bf16 v[4:19], v[72:75], v[108:111], v[4:19]
	v_cvt_pk_bf16_f32 v68, v68, v69
	v_cvt_pk_bf16_f32 v69, v76, v77
	s_waitcnt lgkmcnt(8)
	v_mfma_f32_32x32x16_bf16 v[20:35], v[72:75], v[164:167], v[20:35]
	v_exp_f32_e32 v72, v80
	v_exp_f32_e32 v73, v81
	v_exp_f32_e32 v74, v82
	v_exp_f32_e32 v75, v83
	v_pk_add_f32 v[70:71], v[72:73], v[70:71]
	s_nop 0
	v_pk_add_f32 v[78:79], v[74:75], v[70:71]
	v_cvt_pk_bf16_f32 v70, v72, v73
	v_add_f32_e32 v72, v78, v79
	v_add_f32_e32 v154, v154, v72
	v_cvt_pk_bf16_f32 v71, v74, v75
	s_waitcnt lgkmcnt(6)
	v_mfma_f32_32x32x16_bf16 v[4:19], v[100:103], v[112:115], v[4:19]
	v_max3_f32 v72, v84, v52, v85
	s_nop 0
	v_max3_f32 v72, v72, v53, v86
	s_nop 0
	v_max3_f32 v72, v72, v54, v87
	s_nop 0
	v_max3_f32 v72, v72, v55, v88
	s_waitcnt lgkmcnt(4)
	v_mfma_f32_32x32x16_bf16 v[20:35], v[100:103], v[168:171], v[20:35]
	v_max3_f32 v72, v72, v56, v89
	s_nop 0
	v_max3_f32 v72, v72, v57, v90
	s_nop 0
	v_max3_f32 v72, v72, v58, v91
	s_nop 0
	v_max3_f32 v72, v72, v59, v91
	s_waitcnt lgkmcnt(2)
	v_mfma_f32_32x32x16_bf16 v[4:19], v[68:71], v[156:159], v[4:19]
	s_waitcnt lgkmcnt(0)
	v_mfma_f32_32x32x16_bf16 v[20:35], v[68:71], v[172:175], v[20:35]
	v_max3_f32 v68, v72, v92, v60
	s_nop 0
	v_max3_f32 v68, v68, v93, v61
	s_nop 0
	v_max3_f32 v68, v68, v94, v62
	s_nop 0
	v_max3_f32 v68, v68, v95, v63
	s_nop 0
	v_max3_f32 v68, v68, v96, v64
	s_nop 0
	v_max3_f32 v68, v68, v97, v65
	s_nop 0
	v_max3_f32 v68, v68, v98, v66
	s_nop 0
	v_max3_f32 v68, v68, v99, v67
	s_nop 0
	v_mov_b32_e32 v69, v68
	s_nop 1
	v_permlane32_swap_b32_e32 v68, v69
	s_and_b64 vcc, exec, s[38:39]
	s_cbranch_vccnz .LBB0_1662
	v_max_f32_e32 v68, v68, v68
	v_max_f32_e32 v69, v69, v69
	v_max_f32_e32 v68, v68, v69
	v_cmp_lt_f32_e32 vcc, s13, v68
	s_cbranch_vccz .LBB0_1662
	v_max_f32_e32 v68, v68, v68
	v_max_f32_e32 v68, 0, v68
	v_exp_f32_e64 v69, -v68
	s_and_saveexec_b64 s[6:7], s[36:37]
	s_cbranch_execz .LBB0_1661
	ds_write_b32 v153, v69
	s_branch .LBB0_1661
